# pre-converter image stores write-back (visible through the grid barrier release) instead of write-through; accumulators zeroed in the shadow of the first prologue loads
# speedup vs baseline: 1.0603x; 1.0176x over previous
; #define LAS3 __attribute__((address_space(3)))
; #define G_SCHED __builtin_amdgcn_sched_barrier(0)
; __device__ __forceinline__ int lane_id() { int r; asm volatile("v_mbcnt_lo_u32_b32 %0, -1, 0\n\tv_mbcnt_hi_u32_b32 %0, -1, %0" : "=v"(r)); return r; }
; #define CI_LOAD(R, kt) do { _Pragma("unroll") for (int _j = 0; _j < 16; ++_j) R[_j] = __builtin_nontemporal_load((const f32x4*)(src + (size_t)((kt) * 128 + _j) * LDB)); } while (0)
; template <int LDB>
; __device__ __forceinline__ void convert_image(const float* __restrict__ W, int col0, int col1, unsigned char* __restrict__ img, LAS3 char* lds, int wid) {
;     int lane = lane_id(); asm volatile("" : "+v"(lane));
;     const int n4 = lane, half = n4 >> 5, nloc = (n4 & 31) * 4;
;     const float* src = W + (size_t)(wid * 16) * LDB + ((n4 < 32) ? col0 + n4 * 4 : col1 + (n4 - 32) * 4);
;     const unsigned cpo = (unsigned)(wid * 4096 + lane * 16);
;     ...
;     CI_LOAD(ra, 0);
;     for (int kt = 0; kt < 16; kt += 2) {
;         CI_LOAD(rb, kt + 1); G_SCHED;
.LBB0_75:
	s_cmpk_lg_i32 s80, 0x100
	s_cbranch_scc1 .Lpc_skip
	s_lshr_b32 s1, s35, 3
	s_lshr_b32 s4, s35, 5
	s_add_u32 s1, s1, s4
	s_and_b32 s1, s1, 3
	s_lshr_b32 s0, s87, 8
	s_cmp_lg_u32 s0, s1
	s_cbranch_scc1 .Lpc_skip
	v_readlane_b32 s0, v254, 18
	v_readlane_b32 s1, v254, 19
	s_lshr_b32 s100, s35, 5
	s_and_b32 s101, s35, 31
	s_sub_u32 s88, s101, 16
	s_lshr_b32 s4, s88, 3
	s_lshl_b32 s4, s4, 3
	s_add_u32 s4, s4, s100
	s_and_b32 s5, s88, 7
	s_cmp_lt_u32 s101, 16
	s_cselect_b32 vcc_lo, 1, 0
	s_cselect_b32 s4, s100, s4
	s_cselect_b32 s5, s101, s5
	s_sub_u32 s0, s0, 0x140
	s_subb_u32 s1, s1, 0
	s_lshl_b32 s6, vcc_lo, 4
	s_sub_u32 s6, 0x80, s6
	s_lshl_b32 s88, vcc_lo, 3
	s_sub_u32 s88, 0x120, s88
	s_load_dwordx2 s[100:101], s[0:1], s6
	s_load_dwordx2 s[6:7], s[0:1], s88
	s_load_dwordx2 s[0:1], s[0:1], 0x128
	s_waitcnt lgkmcnt(0)
	s_add_u32 s88, vcc_lo, 24
	s_lshl_b32 s88, s4, s88
	s_add_u32 s100, s100, s88
	s_addc_u32 s101, s101, 0
	s_sub_u32 s88, 10, vcc_lo
	s_lshl_b32 s88, s5, s88
	s_add_u32 s100, s100, s88
	s_addc_u32 s101, s101, 0
	s_lshr_b32 vcc_hi, s75, 6
	s_add_u32 s88, vcc_lo, 17
	s_lshl_b32 s88, vcc_hi, s88
	s_add_u32 s100, s100, s88
	s_addc_u32 s101, s101, 0
	s_add_u32 s88, vcc_lo, 3
	s_lshl_b32 s88, s4, s88
	s_add_u32 s88, s88, s5
	s_lshl_b32 s4, s88, 19
	s_add_u32 s6, s6, s4
	s_addc_u32 s7, s7, 0
	s_xor_b32 s4, vcc_lo, 1
	s_lshl_b32 s4, s4, 9
	s_add_u32 s4, s4, s88
	s_lshl_b32 s4, s4, 2
	s_add_u32 s0, s0, s4
	s_addc_u32 s1, s1, 0
	v_mbcnt_lo_u32_b32 v131, -1, 0
	v_mbcnt_hi_u32_b32 v131, -1, v131
	s_add_u32 s4, vcc_lo, 13
	s_lshl_b32 s5, 1, s4
	s_lshl_b32 s88, vcc_lo, 2
	s_add_u32 s88, s88, 9
	s_lshl_b32 s88, 1, s88
	v_and_b32_e32 v132, 31, v131
	v_lshrrev_b32_e32 v150, 5, v131
	v_lshlrev_b32_e32 v132, 4, v132
	v_mad_u32_u24 v132, v150, s88, v132
	v_add_u32_e32 v133, s5, v132
	v_add_u32_e32 v134, s5, v133
	v_add_u32_e32 v135, s5, v134
	v_add_u32_e32 v136, s5, v135
	v_add_u32_e32 v137, s5, v136
	v_add_u32_e32 v138, s5, v137
	v_add_u32_e32 v139, s5, v138
	v_add_u32_e32 v140, s5, v139
	v_add_u32_e32 v141, s5, v140
	v_add_u32_e32 v142, s5, v141
	v_add_u32_e32 v143, s5, v142
	v_add_u32_e32 v144, s5, v143
	v_add_u32_e32 v145, s5, v144
	v_add_u32_e32 v146, s5, v145
	v_add_u32_e32 v147, s5, v146
	v_and_b32_e32 v151, 3, v131
	v_lshlrev_b32_e32 v151, 1, v151
	v_xor_b32_e32 v148, vcc_hi, v151
	v_or_b32_e32 v151, 1, v151
	v_xor_b32_e32 v149, vcc_hi, v151
	v_lshlrev_b32_e32 v148, 4, v148
	v_lshlrev_b32_e32 v149, 4, v149
	v_and_b32_e32 v151, 31, v131
	v_lshlrev_b32_e32 v151, 9, v151
	v_lshl_add_u32 v151, v150, 14, v151
	v_add_u32_e32 v148, v148, v151
	v_add_u32_e32 v149, v149, v151
	v_add_u32_e32 v149, 0x100, v149
	v_lshlrev_b32_e32 v150, 4, v131
	s_lshl_b32 s4, vcc_hi, 12
	v_add_u32_e32 v150, s4, v150
	s_lshl_b32 s88, s5, 7
	s_mov_b32 s5, 0x3b800000
	global_load_dwordx4 v[0:3], v132, s[100:101] nt
	global_load_dwordx4 v[4:7], v133, s[100:101] nt
	global_load_dwordx4 v[8:11], v134, s[100:101] nt
	global_load_dwordx4 v[12:15], v135, s[100:101] nt
	global_load_dwordx4 v[16:19], v136, s[100:101] nt
	global_load_dwordx4 v[20:23], v137, s[100:101] nt
	global_load_dwordx4 v[24:27], v138, s[100:101] nt
	global_load_dwordx4 v[28:31], v139, s[100:101] nt
	global_load_dwordx4 v[32:35], v140, s[100:101] nt
	global_load_dwordx4 v[36:39], v141, s[100:101] nt
	global_load_dwordx4 v[40:43], v142, s[100:101] nt
	global_load_dwordx4 v[44:47], v143, s[100:101] nt
	global_load_dwordx4 v[48:51], v144, s[100:101] nt
	global_load_dwordx4 v[52:55], v145, s[100:101] nt
	global_load_dwordx4 v[56:59], v146, s[100:101] nt
	global_load_dwordx4 v[60:63], v147, s[100:101] nt
	s_add_u32 s100, s100, s88
	s_addc_u32 s101, s101, 0
	global_load_dwordx4 v[64:67], v132, s[100:101] nt
	global_load_dwordx4 v[68:71], v133, s[100:101] nt
	global_load_dwordx4 v[72:75], v134, s[100:101] nt
	global_load_dwordx4 v[76:79], v135, s[100:101] nt
	global_load_dwordx4 v[80:83], v136, s[100:101] nt
	global_load_dwordx4 v[84:87], v137, s[100:101] nt
	global_load_dwordx4 v[88:91], v138, s[100:101] nt
	global_load_dwordx4 v[92:95], v139, s[100:101] nt
	global_load_dwordx4 v[96:99], v140, s[100:101] nt
	global_load_dwordx4 v[100:103], v141, s[100:101] nt
	global_load_dwordx4 v[104:107], v142, s[100:101] nt
	global_load_dwordx4 v[108:111], v143, s[100:101] nt
	global_load_dwordx4 v[112:115], v144, s[100:101] nt
	global_load_dwordx4 v[116:119], v145, s[100:101] nt
	global_load_dwordx4 v[120:123], v146, s[100:101] nt
	global_load_dwordx4 v[124:127], v147, s[100:101] nt
	s_add_u32 s100, s100, s88
	s_addc_u32 s101, s101, 0
	global_load_dwordx4 v[184:187], v132, s[100:101] nt
	global_load_dwordx4 v[188:191], v133, s[100:101] nt
	global_load_dwordx4 v[192:195], v134, s[100:101] nt
	global_load_dwordx4 v[196:199], v135, s[100:101] nt
	global_load_dwordx4 v[200:203], v136, s[100:101] nt
	global_load_dwordx4 v[204:207], v137, s[100:101] nt
	global_load_dwordx4 v[208:211], v138, s[100:101] nt
	global_load_dwordx4 v[212:215], v139, s[100:101] nt
	global_load_dwordx4 v[216:219], v140, s[100:101] nt
	global_load_dwordx4 v[220:223], v141, s[100:101] nt
	global_load_dwordx4 v[224:227], v142, s[100:101] nt
	global_load_dwordx4 v[228:231], v143, s[100:101] nt
	global_load_dwordx4 v[232:235], v144, s[100:101] nt
	global_load_dwordx4 v[236:239], v145, s[100:101] nt
	global_load_dwordx4 v[240:243], v146, s[100:101] nt
	global_load_dwordx4 v[244:247], v147, s[100:101] nt
	s_waitcnt vmcnt(32)
; #define G_SCHED __builtin_amdgcn_sched_barrier(0)
; #define CI_LOAD(R, kt) do { _Pragma("unroll") for (int _j = 0; _j < 16; ++_j) R[_j] = __builtin_nontemporal_load((const f32x4*)(src + (size_t)((kt) * 128 + _j) * LDB)); } while (0)
; template <int LDB>
; __device__ __forceinline__ void convert_image(const float* __restrict__ W, int col0, int col1, unsigned char* __restrict__ img, LAS3 char* lds, int wid) {
;     ...
;     f32x4 ra[16], rb[16];
;     CI_LOAD(ra, 0);
;     for (int kt = 0; kt < 16; kt += 2) {
;         CI_LOAD(rb, kt + 1); G_SCHED;
;         CI_CONV(ra, kt); G_SCHED;
;         CI_LOAD(ra, (kt + 2 < 16) ? kt + 2 : 15); G_SCHED;
;         CI_CONV(rb, kt + 1); G_SCHED;
;     }
	v_cvt_scalef32_pk_fp8_f32 v152, v0, v4, s5
	v_cvt_scalef32_pk_fp8_f32 v156, v1, v5, s5
	v_cvt_scalef32_pk_fp8_f32 v160, v2, v6, s5
	v_cvt_scalef32_pk_fp8_f32 v164, v3, v7, s5
	v_cvt_scalef32_pk_fp8_f32 v153, v16, v20, s5
	v_cvt_scalef32_pk_fp8_f32 v157, v17, v21, s5
	v_cvt_scalef32_pk_fp8_f32 v161, v18, v22, s5
	v_cvt_scalef32_pk_fp8_f32 v165, v19, v23, s5
	v_cvt_scalef32_pk_fp8_f32 v154, v32, v36, s5
	v_cvt_scalef32_pk_fp8_f32 v158, v33, v37, s5
	v_cvt_scalef32_pk_fp8_f32 v162, v34, v38, s5
	v_cvt_scalef32_pk_fp8_f32 v166, v35, v39, s5
	v_cvt_scalef32_pk_fp8_f32 v155, v48, v52, s5
	v_cvt_scalef32_pk_fp8_f32 v159, v49, v53, s5
	v_cvt_scalef32_pk_fp8_f32 v163, v50, v54, s5
	v_cvt_scalef32_pk_fp8_f32 v167, v51, v55, s5
	v_cvt_scalef32_pk_fp8_f32 v152, v8, v12, s5 op_sel:[0,0,0,1]
	v_cvt_scalef32_pk_fp8_f32 v156, v9, v13, s5 op_sel:[0,0,0,1]
	v_cvt_scalef32_pk_fp8_f32 v160, v10, v14, s5 op_sel:[0,0,0,1]
	v_cvt_scalef32_pk_fp8_f32 v164, v11, v15, s5 op_sel:[0,0,0,1]
	v_cvt_scalef32_pk_fp8_f32 v153, v24, v28, s5 op_sel:[0,0,0,1]
	v_cvt_scalef32_pk_fp8_f32 v157, v25, v29, s5 op_sel:[0,0,0,1]
	v_cvt_scalef32_pk_fp8_f32 v161, v26, v30, s5 op_sel:[0,0,0,1]
	v_cvt_scalef32_pk_fp8_f32 v165, v27, v31, s5 op_sel:[0,0,0,1]
	v_cvt_scalef32_pk_fp8_f32 v154, v40, v44, s5 op_sel:[0,0,0,1]
	v_cvt_scalef32_pk_fp8_f32 v158, v41, v45, s5 op_sel:[0,0,0,1]
	v_cvt_scalef32_pk_fp8_f32 v162, v42, v46, s5 op_sel:[0,0,0,1]
	v_cvt_scalef32_pk_fp8_f32 v166, v43, v47, s5 op_sel:[0,0,0,1]
	v_cvt_scalef32_pk_fp8_f32 v155, v56, v60, s5 op_sel:[0,0,0,1]
	v_cvt_scalef32_pk_fp8_f32 v159, v57, v61, s5 op_sel:[0,0,0,1]
	v_cvt_scalef32_pk_fp8_f32 v163, v58, v62, s5 op_sel:[0,0,0,1]
	v_cvt_scalef32_pk_fp8_f32 v167, v59, v63, s5 op_sel:[0,0,0,1]
	s_add_u32 s100, s100, s88
	s_addc_u32 s101, s101, 0
	global_load_dwordx4 v[0:3], v132, s[100:101] nt
	global_load_dwordx4 v[4:7], v133, s[100:101] nt
	global_load_dwordx4 v[8:11], v134, s[100:101] nt
	global_load_dwordx4 v[12:15], v135, s[100:101] nt
	global_load_dwordx4 v[16:19], v136, s[100:101] nt
	global_load_dwordx4 v[20:23], v137, s[100:101] nt
	global_load_dwordx4 v[24:27], v138, s[100:101] nt
	global_load_dwordx4 v[28:31], v139, s[100:101] nt
	global_load_dwordx4 v[32:35], v140, s[100:101] nt
	global_load_dwordx4 v[36:39], v141, s[100:101] nt
	global_load_dwordx4 v[40:43], v142, s[100:101] nt
	global_load_dwordx4 v[44:47], v143, s[100:101] nt
	global_load_dwordx4 v[48:51], v144, s[100:101] nt
	global_load_dwordx4 v[52:55], v145, s[100:101] nt
	global_load_dwordx4 v[56:59], v146, s[100:101] nt
	global_load_dwordx4 v[60:63], v147, s[100:101] nt
	ds_write_b128 v148, v[152:155] offset:0
	ds_write_b128 v148, v[156:159] offset:128
	ds_write_b128 v149, v[160:163] offset:0
	ds_write_b128 v149, v[164:167] offset:128
	s_waitcnt lgkmcnt(0)
	s_barrier
	ds_read_b128 v[168:171], v150 offset:0
	ds_read_b128 v[172:175], v150 offset:1024
	ds_read_b128 v[176:179], v150 offset:2048
	ds_read_b128 v[180:183], v150 offset:3072
	s_waitcnt lgkmcnt(3)
	global_store_dwordx4 v150, v[168:171], s[6:7] nt
	s_waitcnt lgkmcnt(2)
	global_store_dwordx4 v150, v[172:175], s[6:7] offset:1024 nt
	s_waitcnt lgkmcnt(1)
	global_store_dwordx4 v150, v[176:179], s[6:7] offset:2048 nt
	s_waitcnt lgkmcnt(0)
	global_store_dwordx4 v150, v[180:183], s[6:7] offset:3072 nt
	s_add_u32 s6, s6, 0x8000
	s_addc_u32 s7, s7, 0
	s_waitcnt vmcnt(36)
	v_cvt_scalef32_pk_fp8_f32 v152, v64, v68, s5
	v_cvt_scalef32_pk_fp8_f32 v156, v65, v69, s5
	v_cvt_scalef32_pk_fp8_f32 v160, v66, v70, s5
	v_cvt_scalef32_pk_fp8_f32 v164, v67, v71, s5
	v_cvt_scalef32_pk_fp8_f32 v153, v80, v84, s5
	v_cvt_scalef32_pk_fp8_f32 v157, v81, v85, s5
	v_cvt_scalef32_pk_fp8_f32 v161, v82, v86, s5
	v_cvt_scalef32_pk_fp8_f32 v165, v83, v87, s5
	v_cvt_scalef32_pk_fp8_f32 v154, v96, v100, s5
	v_cvt_scalef32_pk_fp8_f32 v158, v97, v101, s5
	v_cvt_scalef32_pk_fp8_f32 v162, v98, v102, s5
	v_cvt_scalef32_pk_fp8_f32 v166, v99, v103, s5
	v_cvt_scalef32_pk_fp8_f32 v155, v112, v116, s5
	v_cvt_scalef32_pk_fp8_f32 v159, v113, v117, s5
	v_cvt_scalef32_pk_fp8_f32 v163, v114, v118, s5
	v_cvt_scalef32_pk_fp8_f32 v167, v115, v119, s5
	v_cvt_scalef32_pk_fp8_f32 v152, v72, v76, s5 op_sel:[0,0,0,1]
	v_cvt_scalef32_pk_fp8_f32 v156, v73, v77, s5 op_sel:[0,0,0,1]
	v_cvt_scalef32_pk_fp8_f32 v160, v74, v78, s5 op_sel:[0,0,0,1]
	v_cvt_scalef32_pk_fp8_f32 v164, v75, v79, s5 op_sel:[0,0,0,1]
	v_cvt_scalef32_pk_fp8_f32 v153, v88, v92, s5 op_sel:[0,0,0,1]
	v_cvt_scalef32_pk_fp8_f32 v157, v89, v93, s5 op_sel:[0,0,0,1]
	v_cvt_scalef32_pk_fp8_f32 v161, v90, v94, s5 op_sel:[0,0,0,1]
	v_cvt_scalef32_pk_fp8_f32 v165, v91, v95, s5 op_sel:[0,0,0,1]
	v_cvt_scalef32_pk_fp8_f32 v154, v104, v108, s5 op_sel:[0,0,0,1]
	v_cvt_scalef32_pk_fp8_f32 v158, v105, v109, s5 op_sel:[0,0,0,1]
	v_cvt_scalef32_pk_fp8_f32 v162, v106, v110, s5 op_sel:[0,0,0,1]
	v_cvt_scalef32_pk_fp8_f32 v166, v107, v111, s5 op_sel:[0,0,0,1]
	v_cvt_scalef32_pk_fp8_f32 v155, v120, v124, s5 op_sel:[0,0,0,1]
	v_cvt_scalef32_pk_fp8_f32 v159, v121, v125, s5 op_sel:[0,0,0,1]
	v_cvt_scalef32_pk_fp8_f32 v163, v122, v126, s5 op_sel:[0,0,0,1]
	v_cvt_scalef32_pk_fp8_f32 v167, v123, v127, s5 op_sel:[0,0,0,1]
	s_add_u32 s100, s100, s88
	s_addc_u32 s101, s101, 0
	global_load_dwordx4 v[64:67], v132, s[100:101] nt
	global_load_dwordx4 v[68:71], v133, s[100:101] nt
	global_load_dwordx4 v[72:75], v134, s[100:101] nt
	global_load_dwordx4 v[76:79], v135, s[100:101] nt
	global_load_dwordx4 v[80:83], v136, s[100:101] nt
	global_load_dwordx4 v[84:87], v137, s[100:101] nt
	global_load_dwordx4 v[88:91], v138, s[100:101] nt
	global_load_dwordx4 v[92:95], v139, s[100:101] nt
	global_load_dwordx4 v[96:99], v140, s[100:101] nt
	global_load_dwordx4 v[100:103], v141, s[100:101] nt
	global_load_dwordx4 v[104:107], v142, s[100:101] nt
	global_load_dwordx4 v[108:111], v143, s[100:101] nt
	global_load_dwordx4 v[112:115], v144, s[100:101] nt
	global_load_dwordx4 v[116:119], v145, s[100:101] nt
	global_load_dwordx4 v[120:123], v146, s[100:101] nt
	global_load_dwordx4 v[124:127], v147, s[100:101] nt
	ds_write_b128 v148, v[152:155] offset:32768
	ds_write_b128 v148, v[156:159] offset:32896
	ds_write_b128 v149, v[160:163] offset:32768
	ds_write_b128 v149, v[164:167] offset:32896
	s_waitcnt lgkmcnt(0)
	s_barrier
; #define G_SCHED __builtin_amdgcn_sched_barrier(0)
; #define CI_LOAD(R, kt) do { _Pragma("unroll") for (int _j = 0; _j < 16; ++_j) R[_j] = __builtin_nontemporal_load((const f32x4*)(src + (size_t)((kt) * 128 + _j) * LDB)); } while (0)
; template <int LDB>
; __device__ __forceinline__ void convert_image(const float* __restrict__ W, int col0, int col1, unsigned char* __restrict__ img, LAS3 char* lds, int wid) {
;     ...
;     f32x4 ra[16], rb[16];
;     CI_LOAD(ra, 0);
;     for (int kt = 0; kt < 16; kt += 2) {
;         CI_LOAD(rb, kt + 1); G_SCHED;
;         CI_CONV(ra, kt); G_SCHED;
;         CI_LOAD(ra, (kt + 2 < 16) ? kt + 2 : 15); G_SCHED;
;         CI_CONV(rb, kt + 1); G_SCHED;
;     }
	ds_read_b128 v[168:171], v150 offset:32768
	ds_read_b128 v[172:175], v150 offset:33792
	ds_read_b128 v[176:179], v150 offset:34816
	ds_read_b128 v[180:183], v150 offset:35840
	s_waitcnt lgkmcnt(3)
	global_store_dwordx4 v150, v[168:171], s[6:7] nt
	s_waitcnt lgkmcnt(2)
	global_store_dwordx4 v150, v[172:175], s[6:7] offset:1024 nt
	s_waitcnt lgkmcnt(1)
	global_store_dwordx4 v150, v[176:179], s[6:7] offset:2048 nt
	s_waitcnt lgkmcnt(0)
	global_store_dwordx4 v150, v[180:183], s[6:7] offset:3072 nt
	s_add_u32 s6, s6, 0x8000
	s_addc_u32 s7, s7, 0
	s_waitcnt vmcnt(40)
	v_cvt_scalef32_pk_fp8_f32 v152, v184, v188, s5
	v_cvt_scalef32_pk_fp8_f32 v156, v185, v189, s5
	v_cvt_scalef32_pk_fp8_f32 v160, v186, v190, s5
	v_cvt_scalef32_pk_fp8_f32 v164, v187, v191, s5
	v_cvt_scalef32_pk_fp8_f32 v153, v200, v204, s5
	v_cvt_scalef32_pk_fp8_f32 v157, v201, v205, s5
	v_cvt_scalef32_pk_fp8_f32 v161, v202, v206, s5
	v_cvt_scalef32_pk_fp8_f32 v165, v203, v207, s5
	v_cvt_scalef32_pk_fp8_f32 v154, v216, v220, s5
	v_cvt_scalef32_pk_fp8_f32 v158, v217, v221, s5
	v_cvt_scalef32_pk_fp8_f32 v162, v218, v222, s5
	v_cvt_scalef32_pk_fp8_f32 v166, v219, v223, s5
	v_cvt_scalef32_pk_fp8_f32 v155, v232, v236, s5
	v_cvt_scalef32_pk_fp8_f32 v159, v233, v237, s5
	v_cvt_scalef32_pk_fp8_f32 v163, v234, v238, s5
	v_cvt_scalef32_pk_fp8_f32 v167, v235, v239, s5
	v_cvt_scalef32_pk_fp8_f32 v152, v192, v196, s5 op_sel:[0,0,0,1]
	v_cvt_scalef32_pk_fp8_f32 v156, v193, v197, s5 op_sel:[0,0,0,1]
	v_cvt_scalef32_pk_fp8_f32 v160, v194, v198, s5 op_sel:[0,0,0,1]
	v_cvt_scalef32_pk_fp8_f32 v164, v195, v199, s5 op_sel:[0,0,0,1]
	v_cvt_scalef32_pk_fp8_f32 v153, v208, v212, s5 op_sel:[0,0,0,1]
	v_cvt_scalef32_pk_fp8_f32 v157, v209, v213, s5 op_sel:[0,0,0,1]
	v_cvt_scalef32_pk_fp8_f32 v161, v210, v214, s5 op_sel:[0,0,0,1]
	v_cvt_scalef32_pk_fp8_f32 v165, v211, v215, s5 op_sel:[0,0,0,1]
	v_cvt_scalef32_pk_fp8_f32 v154, v224, v228, s5 op_sel:[0,0,0,1]
	v_cvt_scalef32_pk_fp8_f32 v158, v225, v229, s5 op_sel:[0,0,0,1]
	v_cvt_scalef32_pk_fp8_f32 v162, v226, v230, s5 op_sel:[0,0,0,1]
	v_cvt_scalef32_pk_fp8_f32 v166, v227, v231, s5 op_sel:[0,0,0,1]
	v_cvt_scalef32_pk_fp8_f32 v155, v240, v244, s5 op_sel:[0,0,0,1]
	v_cvt_scalef32_pk_fp8_f32 v159, v241, v245, s5 op_sel:[0,0,0,1]
	v_cvt_scalef32_pk_fp8_f32 v163, v242, v246, s5 op_sel:[0,0,0,1]
	v_cvt_scalef32_pk_fp8_f32 v167, v243, v247, s5 op_sel:[0,0,0,1]
	s_add_u32 s100, s100, s88
	s_addc_u32 s101, s101, 0
	global_load_dwordx4 v[184:187], v132, s[100:101] nt
	global_load_dwordx4 v[188:191], v133, s[100:101] nt
	global_load_dwordx4 v[192:195], v134, s[100:101] nt
	global_load_dwordx4 v[196:199], v135, s[100:101] nt
	global_load_dwordx4 v[200:203], v136, s[100:101] nt
	global_load_dwordx4 v[204:207], v137, s[100:101] nt
	global_load_dwordx4 v[208:211], v138, s[100:101] nt
	global_load_dwordx4 v[212:215], v139, s[100:101] nt
	global_load_dwordx4 v[216:219], v140, s[100:101] nt
	global_load_dwordx4 v[220:223], v141, s[100:101] nt
	global_load_dwordx4 v[224:227], v142, s[100:101] nt
	global_load_dwordx4 v[228:231], v143, s[100:101] nt
	global_load_dwordx4 v[232:235], v144, s[100:101] nt
	global_load_dwordx4 v[236:239], v145, s[100:101] nt
	global_load_dwordx4 v[240:243], v146, s[100:101] nt
	global_load_dwordx4 v[244:247], v147, s[100:101] nt
	ds_write_b128 v148, v[152:155] offset:0
	ds_write_b128 v148, v[156:159] offset:128
	ds_write_b128 v149, v[160:163] offset:0
	ds_write_b128 v149, v[164:167] offset:128
	s_waitcnt lgkmcnt(0)
	s_barrier
	ds_read_b128 v[168:171], v150 offset:0
	ds_read_b128 v[172:175], v150 offset:1024
	ds_read_b128 v[176:179], v150 offset:2048
	ds_read_b128 v[180:183], v150 offset:3072
	s_waitcnt lgkmcnt(3)
	global_store_dwordx4 v150, v[168:171], s[6:7] nt
	s_waitcnt lgkmcnt(2)
	global_store_dwordx4 v150, v[172:175], s[6:7] offset:1024 nt
	s_waitcnt lgkmcnt(1)
	global_store_dwordx4 v150, v[176:179], s[6:7] offset:2048 nt
	s_waitcnt lgkmcnt(0)
	global_store_dwordx4 v150, v[180:183], s[6:7] offset:3072 nt
	s_add_u32 s6, s6, 0x8000
	s_addc_u32 s7, s7, 0
	s_waitcnt vmcnt(44)
	v_cvt_scalef32_pk_fp8_f32 v152, v0, v4, s5
	v_cvt_scalef32_pk_fp8_f32 v156, v1, v5, s5
	v_cvt_scalef32_pk_fp8_f32 v160, v2, v6, s5
	v_cvt_scalef32_pk_fp8_f32 v164, v3, v7, s5
	v_cvt_scalef32_pk_fp8_f32 v153, v16, v20, s5
	v_cvt_scalef32_pk_fp8_f32 v157, v17, v21, s5
	v_cvt_scalef32_pk_fp8_f32 v161, v18, v22, s5
	v_cvt_scalef32_pk_fp8_f32 v165, v19, v23, s5
	v_cvt_scalef32_pk_fp8_f32 v154, v32, v36, s5
	v_cvt_scalef32_pk_fp8_f32 v158, v33, v37, s5
	v_cvt_scalef32_pk_fp8_f32 v162, v34, v38, s5
	v_cvt_scalef32_pk_fp8_f32 v166, v35, v39, s5
	v_cvt_scalef32_pk_fp8_f32 v155, v48, v52, s5
	v_cvt_scalef32_pk_fp8_f32 v159, v49, v53, s5
	v_cvt_scalef32_pk_fp8_f32 v163, v50, v54, s5
	v_cvt_scalef32_pk_fp8_f32 v167, v51, v55, s5
	v_cvt_scalef32_pk_fp8_f32 v152, v8, v12, s5 op_sel:[0,0,0,1]
	v_cvt_scalef32_pk_fp8_f32 v156, v9, v13, s5 op_sel:[0,0,0,1]
	v_cvt_scalef32_pk_fp8_f32 v160, v10, v14, s5 op_sel:[0,0,0,1]
	v_cvt_scalef32_pk_fp8_f32 v164, v11, v15, s5 op_sel:[0,0,0,1]
	v_cvt_scalef32_pk_fp8_f32 v153, v24, v28, s5 op_sel:[0,0,0,1]
	v_cvt_scalef32_pk_fp8_f32 v157, v25, v29, s5 op_sel:[0,0,0,1]
	v_cvt_scalef32_pk_fp8_f32 v161, v26, v30, s5 op_sel:[0,0,0,1]
	v_cvt_scalef32_pk_fp8_f32 v165, v27, v31, s5 op_sel:[0,0,0,1]
	v_cvt_scalef32_pk_fp8_f32 v154, v40, v44, s5 op_sel:[0,0,0,1]
	v_cvt_scalef32_pk_fp8_f32 v158, v41, v45, s5 op_sel:[0,0,0,1]
	v_cvt_scalef32_pk_fp8_f32 v162, v42, v46, s5 op_sel:[0,0,0,1]
	v_cvt_scalef32_pk_fp8_f32 v166, v43, v47, s5 op_sel:[0,0,0,1]
	v_cvt_scalef32_pk_fp8_f32 v155, v56, v60, s5 op_sel:[0,0,0,1]
	v_cvt_scalef32_pk_fp8_f32 v159, v57, v61, s5 op_sel:[0,0,0,1]
	v_cvt_scalef32_pk_fp8_f32 v163, v58, v62, s5 op_sel:[0,0,0,1]
	v_cvt_scalef32_pk_fp8_f32 v167, v59, v63, s5 op_sel:[0,0,0,1]
	s_add_u32 s100, s100, s88
	s_addc_u32 s101, s101, 0
	global_load_dwordx4 v[0:3], v132, s[100:101] nt
	global_load_dwordx4 v[4:7], v133, s[100:101] nt
	global_load_dwordx4 v[8:11], v134, s[100:101] nt
	global_load_dwordx4 v[12:15], v135, s[100:101] nt
	global_load_dwordx4 v[16:19], v136, s[100:101] nt
	global_load_dwordx4 v[20:23], v137, s[100:101] nt
	global_load_dwordx4 v[24:27], v138, s[100:101] nt
	global_load_dwordx4 v[28:31], v139, s[100:101] nt
	global_load_dwordx4 v[32:35], v140, s[100:101] nt
	global_load_dwordx4 v[36:39], v141, s[100:101] nt
	global_load_dwordx4 v[40:43], v142, s[100:101] nt
	global_load_dwordx4 v[44:47], v143, s[100:101] nt
	global_load_dwordx4 v[48:51], v144, s[100:101] nt
	global_load_dwordx4 v[52:55], v145, s[100:101] nt
	global_load_dwordx4 v[56:59], v146, s[100:101] nt
	global_load_dwordx4 v[60:63], v147, s[100:101] nt
	ds_write_b128 v148, v[152:155] offset:32768
	ds_write_b128 v148, v[156:159] offset:32896
	ds_write_b128 v149, v[160:163] offset:32768
	ds_write_b128 v149, v[164:167] offset:32896
	s_waitcnt lgkmcnt(0)
	s_barrier
; #define G_SCHED __builtin_amdgcn_sched_barrier(0)
; #define CI_LOAD(R, kt) do { _Pragma("unroll") for (int _j = 0; _j < 16; ++_j) R[_j] = __builtin_nontemporal_load((const f32x4*)(src + (size_t)((kt) * 128 + _j) * LDB)); } while (0)
; template <int LDB>
; __device__ __forceinline__ void convert_image(const float* __restrict__ W, int col0, int col1, unsigned char* __restrict__ img, LAS3 char* lds, int wid) {
;     ...
;     f32x4 ra[16], rb[16];
;     CI_LOAD(ra, 0);
;     for (int kt = 0; kt < 16; kt += 2) {
;         CI_LOAD(rb, kt + 1); G_SCHED;
;         CI_CONV(ra, kt); G_SCHED;
;         CI_LOAD(ra, (kt + 2 < 16) ? kt + 2 : 15); G_SCHED;
;         CI_CONV(rb, kt + 1); G_SCHED;
;     }
	ds_read_b128 v[168:171], v150 offset:32768
	ds_read_b128 v[172:175], v150 offset:33792
	ds_read_b128 v[176:179], v150 offset:34816
	ds_read_b128 v[180:183], v150 offset:35840
	s_waitcnt lgkmcnt(3)
	global_store_dwordx4 v150, v[168:171], s[6:7] nt
	s_waitcnt lgkmcnt(2)
	global_store_dwordx4 v150, v[172:175], s[6:7] offset:1024 nt
	s_waitcnt lgkmcnt(1)
	global_store_dwordx4 v150, v[176:179], s[6:7] offset:2048 nt
	s_waitcnt lgkmcnt(0)
	global_store_dwordx4 v150, v[180:183], s[6:7] offset:3072 nt
	s_add_u32 s6, s6, 0x8000
	s_addc_u32 s7, s7, 0
	s_waitcnt vmcnt(44)
	v_cvt_scalef32_pk_fp8_f32 v152, v64, v68, s5
	v_cvt_scalef32_pk_fp8_f32 v156, v65, v69, s5
	v_cvt_scalef32_pk_fp8_f32 v160, v66, v70, s5
	v_cvt_scalef32_pk_fp8_f32 v164, v67, v71, s5
	v_cvt_scalef32_pk_fp8_f32 v153, v80, v84, s5
	v_cvt_scalef32_pk_fp8_f32 v157, v81, v85, s5
	v_cvt_scalef32_pk_fp8_f32 v161, v82, v86, s5
	v_cvt_scalef32_pk_fp8_f32 v165, v83, v87, s5
	v_cvt_scalef32_pk_fp8_f32 v154, v96, v100, s5
	v_cvt_scalef32_pk_fp8_f32 v158, v97, v101, s5
	v_cvt_scalef32_pk_fp8_f32 v162, v98, v102, s5
	v_cvt_scalef32_pk_fp8_f32 v166, v99, v103, s5
	v_cvt_scalef32_pk_fp8_f32 v155, v112, v116, s5
	v_cvt_scalef32_pk_fp8_f32 v159, v113, v117, s5
	v_cvt_scalef32_pk_fp8_f32 v163, v114, v118, s5
	v_cvt_scalef32_pk_fp8_f32 v167, v115, v119, s5
	v_cvt_scalef32_pk_fp8_f32 v152, v72, v76, s5 op_sel:[0,0,0,1]
	v_cvt_scalef32_pk_fp8_f32 v156, v73, v77, s5 op_sel:[0,0,0,1]
	v_cvt_scalef32_pk_fp8_f32 v160, v74, v78, s5 op_sel:[0,0,0,1]
	v_cvt_scalef32_pk_fp8_f32 v164, v75, v79, s5 op_sel:[0,0,0,1]
	v_cvt_scalef32_pk_fp8_f32 v153, v88, v92, s5 op_sel:[0,0,0,1]
	v_cvt_scalef32_pk_fp8_f32 v157, v89, v93, s5 op_sel:[0,0,0,1]
	v_cvt_scalef32_pk_fp8_f32 v161, v90, v94, s5 op_sel:[0,0,0,1]
	v_cvt_scalef32_pk_fp8_f32 v165, v91, v95, s5 op_sel:[0,0,0,1]
	v_cvt_scalef32_pk_fp8_f32 v154, v104, v108, s5 op_sel:[0,0,0,1]
	v_cvt_scalef32_pk_fp8_f32 v158, v105, v109, s5 op_sel:[0,0,0,1]
	v_cvt_scalef32_pk_fp8_f32 v162, v106, v110, s5 op_sel:[0,0,0,1]
	v_cvt_scalef32_pk_fp8_f32 v166, v107, v111, s5 op_sel:[0,0,0,1]
	v_cvt_scalef32_pk_fp8_f32 v155, v120, v124, s5 op_sel:[0,0,0,1]
	v_cvt_scalef32_pk_fp8_f32 v159, v121, v125, s5 op_sel:[0,0,0,1]
	v_cvt_scalef32_pk_fp8_f32 v163, v122, v126, s5 op_sel:[0,0,0,1]
	v_cvt_scalef32_pk_fp8_f32 v167, v123, v127, s5 op_sel:[0,0,0,1]
	s_add_u32 s100, s100, s88
	s_addc_u32 s101, s101, 0
	global_load_dwordx4 v[64:67], v132, s[100:101] nt
	global_load_dwordx4 v[68:71], v133, s[100:101] nt
	global_load_dwordx4 v[72:75], v134, s[100:101] nt
	global_load_dwordx4 v[76:79], v135, s[100:101] nt
	global_load_dwordx4 v[80:83], v136, s[100:101] nt
	global_load_dwordx4 v[84:87], v137, s[100:101] nt
	global_load_dwordx4 v[88:91], v138, s[100:101] nt
	global_load_dwordx4 v[92:95], v139, s[100:101] nt
	global_load_dwordx4 v[96:99], v140, s[100:101] nt
	global_load_dwordx4 v[100:103], v141, s[100:101] nt
	global_load_dwordx4 v[104:107], v142, s[100:101] nt
	global_load_dwordx4 v[108:111], v143, s[100:101] nt
	global_load_dwordx4 v[112:115], v144, s[100:101] nt
	global_load_dwordx4 v[116:119], v145, s[100:101] nt
	global_load_dwordx4 v[120:123], v146, s[100:101] nt
	global_load_dwordx4 v[124:127], v147, s[100:101] nt
	ds_write_b128 v148, v[152:155] offset:0
	ds_write_b128 v148, v[156:159] offset:128
	ds_write_b128 v149, v[160:163] offset:0
	ds_write_b128 v149, v[164:167] offset:128
	s_waitcnt lgkmcnt(0)
	s_barrier
	ds_read_b128 v[168:171], v150 offset:0
	ds_read_b128 v[172:175], v150 offset:1024
	ds_read_b128 v[176:179], v150 offset:2048
	ds_read_b128 v[180:183], v150 offset:3072
	s_waitcnt lgkmcnt(3)
	global_store_dwordx4 v150, v[168:171], s[6:7] nt
	s_waitcnt lgkmcnt(2)
	global_store_dwordx4 v150, v[172:175], s[6:7] offset:1024 nt
	s_waitcnt lgkmcnt(1)
	global_store_dwordx4 v150, v[176:179], s[6:7] offset:2048 nt
	s_waitcnt lgkmcnt(0)
	global_store_dwordx4 v150, v[180:183], s[6:7] offset:3072 nt
	s_add_u32 s6, s6, 0x8000
	s_addc_u32 s7, s7, 0
	s_waitcnt vmcnt(44)
	v_cvt_scalef32_pk_fp8_f32 v152, v184, v188, s5
	v_cvt_scalef32_pk_fp8_f32 v156, v185, v189, s5
	v_cvt_scalef32_pk_fp8_f32 v160, v186, v190, s5
	v_cvt_scalef32_pk_fp8_f32 v164, v187, v191, s5
	v_cvt_scalef32_pk_fp8_f32 v153, v200, v204, s5
	v_cvt_scalef32_pk_fp8_f32 v157, v201, v205, s5
	v_cvt_scalef32_pk_fp8_f32 v161, v202, v206, s5
	v_cvt_scalef32_pk_fp8_f32 v165, v203, v207, s5
	v_cvt_scalef32_pk_fp8_f32 v154, v216, v220, s5
	v_cvt_scalef32_pk_fp8_f32 v158, v217, v221, s5
	v_cvt_scalef32_pk_fp8_f32 v162, v218, v222, s5
	v_cvt_scalef32_pk_fp8_f32 v166, v219, v223, s5
	v_cvt_scalef32_pk_fp8_f32 v155, v232, v236, s5
	v_cvt_scalef32_pk_fp8_f32 v159, v233, v237, s5
	v_cvt_scalef32_pk_fp8_f32 v163, v234, v238, s5
	v_cvt_scalef32_pk_fp8_f32 v167, v235, v239, s5
	v_cvt_scalef32_pk_fp8_f32 v152, v192, v196, s5 op_sel:[0,0,0,1]
	v_cvt_scalef32_pk_fp8_f32 v156, v193, v197, s5 op_sel:[0,0,0,1]
	v_cvt_scalef32_pk_fp8_f32 v160, v194, v198, s5 op_sel:[0,0,0,1]
	v_cvt_scalef32_pk_fp8_f32 v164, v195, v199, s5 op_sel:[0,0,0,1]
	v_cvt_scalef32_pk_fp8_f32 v153, v208, v212, s5 op_sel:[0,0,0,1]
	v_cvt_scalef32_pk_fp8_f32 v157, v209, v213, s5 op_sel:[0,0,0,1]
	v_cvt_scalef32_pk_fp8_f32 v161, v210, v214, s5 op_sel:[0,0,0,1]
	v_cvt_scalef32_pk_fp8_f32 v165, v211, v215, s5 op_sel:[0,0,0,1]
	v_cvt_scalef32_pk_fp8_f32 v154, v224, v228, s5 op_sel:[0,0,0,1]
	v_cvt_scalef32_pk_fp8_f32 v158, v225, v229, s5 op_sel:[0,0,0,1]
	v_cvt_scalef32_pk_fp8_f32 v162, v226, v230, s5 op_sel:[0,0,0,1]
	v_cvt_scalef32_pk_fp8_f32 v166, v227, v231, s5 op_sel:[0,0,0,1]
	v_cvt_scalef32_pk_fp8_f32 v155, v240, v244, s5 op_sel:[0,0,0,1]
	v_cvt_scalef32_pk_fp8_f32 v159, v241, v245, s5 op_sel:[0,0,0,1]
	v_cvt_scalef32_pk_fp8_f32 v163, v242, v246, s5 op_sel:[0,0,0,1]
	v_cvt_scalef32_pk_fp8_f32 v167, v243, v247, s5 op_sel:[0,0,0,1]
	s_add_u32 s100, s100, s88
	s_addc_u32 s101, s101, 0
	global_load_dwordx4 v[184:187], v132, s[100:101] nt
	global_load_dwordx4 v[188:191], v133, s[100:101] nt
	global_load_dwordx4 v[192:195], v134, s[100:101] nt
	global_load_dwordx4 v[196:199], v135, s[100:101] nt
	global_load_dwordx4 v[200:203], v136, s[100:101] nt
	global_load_dwordx4 v[204:207], v137, s[100:101] nt
	global_load_dwordx4 v[208:211], v138, s[100:101] nt
	global_load_dwordx4 v[212:215], v139, s[100:101] nt
	global_load_dwordx4 v[216:219], v140, s[100:101] nt
	global_load_dwordx4 v[220:223], v141, s[100:101] nt
	global_load_dwordx4 v[224:227], v142, s[100:101] nt
	global_load_dwordx4 v[228:231], v143, s[100:101] nt
	global_load_dwordx4 v[232:235], v144, s[100:101] nt
	global_load_dwordx4 v[236:239], v145, s[100:101] nt
	global_load_dwordx4 v[240:243], v146, s[100:101] nt
	global_load_dwordx4 v[244:247], v147, s[100:101] nt
	ds_write_b128 v148, v[152:155] offset:32768
	ds_write_b128 v148, v[156:159] offset:32896
	ds_write_b128 v149, v[160:163] offset:32768
	ds_write_b128 v149, v[164:167] offset:32896
	s_waitcnt lgkmcnt(0)
	s_barrier
; #define G_SCHED __builtin_amdgcn_sched_barrier(0)
; #define CI_LOAD(R, kt) do { _Pragma("unroll") for (int _j = 0; _j < 16; ++_j) R[_j] = __builtin_nontemporal_load((const f32x4*)(src + (size_t)((kt) * 128 + _j) * LDB)); } while (0)
; template <int LDB>
; __device__ __forceinline__ void convert_image(const float* __restrict__ W, int col0, int col1, unsigned char* __restrict__ img, LAS3 char* lds, int wid) {
;     ...
;     f32x4 ra[16], rb[16];
;     CI_LOAD(ra, 0);
;     for (int kt = 0; kt < 16; kt += 2) {
;         CI_LOAD(rb, kt + 1); G_SCHED;
;         CI_CONV(ra, kt); G_SCHED;
;         CI_LOAD(ra, (kt + 2 < 16) ? kt + 2 : 15); G_SCHED;
;         CI_CONV(rb, kt + 1); G_SCHED;
;     }
	ds_read_b128 v[168:171], v150 offset:32768
	ds_read_b128 v[172:175], v150 offset:33792
	ds_read_b128 v[176:179], v150 offset:34816
	ds_read_b128 v[180:183], v150 offset:35840
	s_waitcnt lgkmcnt(3)
	global_store_dwordx4 v150, v[168:171], s[6:7] nt
	s_waitcnt lgkmcnt(2)
	global_store_dwordx4 v150, v[172:175], s[6:7] offset:1024 nt
	s_waitcnt lgkmcnt(1)
	global_store_dwordx4 v150, v[176:179], s[6:7] offset:2048 nt
	s_waitcnt lgkmcnt(0)
	global_store_dwordx4 v150, v[180:183], s[6:7] offset:3072 nt
	s_add_u32 s6, s6, 0x8000
	s_addc_u32 s7, s7, 0
	s_waitcnt vmcnt(44)
	v_cvt_scalef32_pk_fp8_f32 v152, v0, v4, s5
	v_cvt_scalef32_pk_fp8_f32 v156, v1, v5, s5
	v_cvt_scalef32_pk_fp8_f32 v160, v2, v6, s5
	v_cvt_scalef32_pk_fp8_f32 v164, v3, v7, s5
	v_cvt_scalef32_pk_fp8_f32 v153, v16, v20, s5
	v_cvt_scalef32_pk_fp8_f32 v157, v17, v21, s5
	v_cvt_scalef32_pk_fp8_f32 v161, v18, v22, s5
	v_cvt_scalef32_pk_fp8_f32 v165, v19, v23, s5
	v_cvt_scalef32_pk_fp8_f32 v154, v32, v36, s5
	v_cvt_scalef32_pk_fp8_f32 v158, v33, v37, s5
	v_cvt_scalef32_pk_fp8_f32 v162, v34, v38, s5
	v_cvt_scalef32_pk_fp8_f32 v166, v35, v39, s5
	v_cvt_scalef32_pk_fp8_f32 v155, v48, v52, s5
	v_cvt_scalef32_pk_fp8_f32 v159, v49, v53, s5
	v_cvt_scalef32_pk_fp8_f32 v163, v50, v54, s5
	v_cvt_scalef32_pk_fp8_f32 v167, v51, v55, s5
	v_cvt_scalef32_pk_fp8_f32 v152, v8, v12, s5 op_sel:[0,0,0,1]
	v_cvt_scalef32_pk_fp8_f32 v156, v9, v13, s5 op_sel:[0,0,0,1]
	v_cvt_scalef32_pk_fp8_f32 v160, v10, v14, s5 op_sel:[0,0,0,1]
	v_cvt_scalef32_pk_fp8_f32 v164, v11, v15, s5 op_sel:[0,0,0,1]
	v_cvt_scalef32_pk_fp8_f32 v153, v24, v28, s5 op_sel:[0,0,0,1]
	v_cvt_scalef32_pk_fp8_f32 v157, v25, v29, s5 op_sel:[0,0,0,1]
	v_cvt_scalef32_pk_fp8_f32 v161, v26, v30, s5 op_sel:[0,0,0,1]
	v_cvt_scalef32_pk_fp8_f32 v165, v27, v31, s5 op_sel:[0,0,0,1]
	v_cvt_scalef32_pk_fp8_f32 v154, v40, v44, s5 op_sel:[0,0,0,1]
	v_cvt_scalef32_pk_fp8_f32 v158, v41, v45, s5 op_sel:[0,0,0,1]
	v_cvt_scalef32_pk_fp8_f32 v162, v42, v46, s5 op_sel:[0,0,0,1]
	v_cvt_scalef32_pk_fp8_f32 v166, v43, v47, s5 op_sel:[0,0,0,1]
	v_cvt_scalef32_pk_fp8_f32 v155, v56, v60, s5 op_sel:[0,0,0,1]
	v_cvt_scalef32_pk_fp8_f32 v159, v57, v61, s5 op_sel:[0,0,0,1]
	v_cvt_scalef32_pk_fp8_f32 v163, v58, v62, s5 op_sel:[0,0,0,1]
	v_cvt_scalef32_pk_fp8_f32 v167, v59, v63, s5 op_sel:[0,0,0,1]
	s_add_u32 s100, s100, s88
	s_addc_u32 s101, s101, 0
	global_load_dwordx4 v[0:3], v132, s[100:101] nt
	global_load_dwordx4 v[4:7], v133, s[100:101] nt
	global_load_dwordx4 v[8:11], v134, s[100:101] nt
	global_load_dwordx4 v[12:15], v135, s[100:101] nt
	global_load_dwordx4 v[16:19], v136, s[100:101] nt
	global_load_dwordx4 v[20:23], v137, s[100:101] nt
	global_load_dwordx4 v[24:27], v138, s[100:101] nt
	global_load_dwordx4 v[28:31], v139, s[100:101] nt
	global_load_dwordx4 v[32:35], v140, s[100:101] nt
	global_load_dwordx4 v[36:39], v141, s[100:101] nt
	global_load_dwordx4 v[40:43], v142, s[100:101] nt
	global_load_dwordx4 v[44:47], v143, s[100:101] nt
	global_load_dwordx4 v[48:51], v144, s[100:101] nt
	global_load_dwordx4 v[52:55], v145, s[100:101] nt
	global_load_dwordx4 v[56:59], v146, s[100:101] nt
	global_load_dwordx4 v[60:63], v147, s[100:101] nt
	ds_write_b128 v148, v[152:155] offset:0
	ds_write_b128 v148, v[156:159] offset:128
	ds_write_b128 v149, v[160:163] offset:0
	ds_write_b128 v149, v[164:167] offset:128
	s_waitcnt lgkmcnt(0)
	s_barrier
	ds_read_b128 v[168:171], v150 offset:0
	ds_read_b128 v[172:175], v150 offset:1024
	ds_read_b128 v[176:179], v150 offset:2048
	ds_read_b128 v[180:183], v150 offset:3072
	s_waitcnt lgkmcnt(3)
	global_store_dwordx4 v150, v[168:171], s[6:7] nt
	s_waitcnt lgkmcnt(2)
	global_store_dwordx4 v150, v[172:175], s[6:7] offset:1024 nt
	s_waitcnt lgkmcnt(1)
	global_store_dwordx4 v150, v[176:179], s[6:7] offset:2048 nt
	s_waitcnt lgkmcnt(0)
	global_store_dwordx4 v150, v[180:183], s[6:7] offset:3072 nt
	s_add_u32 s6, s6, 0x8000
	s_addc_u32 s7, s7, 0
	s_waitcnt vmcnt(44)
	v_cvt_scalef32_pk_fp8_f32 v152, v64, v68, s5
	v_cvt_scalef32_pk_fp8_f32 v156, v65, v69, s5
	v_cvt_scalef32_pk_fp8_f32 v160, v66, v70, s5
	v_cvt_scalef32_pk_fp8_f32 v164, v67, v71, s5
	v_cvt_scalef32_pk_fp8_f32 v153, v80, v84, s5
	v_cvt_scalef32_pk_fp8_f32 v157, v81, v85, s5
	v_cvt_scalef32_pk_fp8_f32 v161, v82, v86, s5
	v_cvt_scalef32_pk_fp8_f32 v165, v83, v87, s5
	v_cvt_scalef32_pk_fp8_f32 v154, v96, v100, s5
	v_cvt_scalef32_pk_fp8_f32 v158, v97, v101, s5
	v_cvt_scalef32_pk_fp8_f32 v162, v98, v102, s5
	v_cvt_scalef32_pk_fp8_f32 v166, v99, v103, s5
	v_cvt_scalef32_pk_fp8_f32 v155, v112, v116, s5
	v_cvt_scalef32_pk_fp8_f32 v159, v113, v117, s5
	v_cvt_scalef32_pk_fp8_f32 v163, v114, v118, s5
	v_cvt_scalef32_pk_fp8_f32 v167, v115, v119, s5
	v_cvt_scalef32_pk_fp8_f32 v152, v72, v76, s5 op_sel:[0,0,0,1]
	v_cvt_scalef32_pk_fp8_f32 v156, v73, v77, s5 op_sel:[0,0,0,1]
	v_cvt_scalef32_pk_fp8_f32 v160, v74, v78, s5 op_sel:[0,0,0,1]
	v_cvt_scalef32_pk_fp8_f32 v164, v75, v79, s5 op_sel:[0,0,0,1]
	v_cvt_scalef32_pk_fp8_f32 v153, v88, v92, s5 op_sel:[0,0,0,1]
	v_cvt_scalef32_pk_fp8_f32 v157, v89, v93, s5 op_sel:[0,0,0,1]
	v_cvt_scalef32_pk_fp8_f32 v161, v90, v94, s5 op_sel:[0,0,0,1]
	v_cvt_scalef32_pk_fp8_f32 v165, v91, v95, s5 op_sel:[0,0,0,1]
	v_cvt_scalef32_pk_fp8_f32 v154, v104, v108, s5 op_sel:[0,0,0,1]
	v_cvt_scalef32_pk_fp8_f32 v158, v105, v109, s5 op_sel:[0,0,0,1]
	v_cvt_scalef32_pk_fp8_f32 v162, v106, v110, s5 op_sel:[0,0,0,1]
	v_cvt_scalef32_pk_fp8_f32 v166, v107, v111, s5 op_sel:[0,0,0,1]
	v_cvt_scalef32_pk_fp8_f32 v155, v120, v124, s5 op_sel:[0,0,0,1]
	v_cvt_scalef32_pk_fp8_f32 v159, v121, v125, s5 op_sel:[0,0,0,1]
	v_cvt_scalef32_pk_fp8_f32 v163, v122, v126, s5 op_sel:[0,0,0,1]
	v_cvt_scalef32_pk_fp8_f32 v167, v123, v127, s5 op_sel:[0,0,0,1]
	s_add_u32 s100, s100, s88
	s_addc_u32 s101, s101, 0
	global_load_dwordx4 v[64:67], v132, s[100:101] nt
	global_load_dwordx4 v[68:71], v133, s[100:101] nt
	global_load_dwordx4 v[72:75], v134, s[100:101] nt
	global_load_dwordx4 v[76:79], v135, s[100:101] nt
	global_load_dwordx4 v[80:83], v136, s[100:101] nt
	global_load_dwordx4 v[84:87], v137, s[100:101] nt
	global_load_dwordx4 v[88:91], v138, s[100:101] nt
	global_load_dwordx4 v[92:95], v139, s[100:101] nt
	global_load_dwordx4 v[96:99], v140, s[100:101] nt
	global_load_dwordx4 v[100:103], v141, s[100:101] nt
	global_load_dwordx4 v[104:107], v142, s[100:101] nt
	global_load_dwordx4 v[108:111], v143, s[100:101] nt
	global_load_dwordx4 v[112:115], v144, s[100:101] nt
	global_load_dwordx4 v[116:119], v145, s[100:101] nt
	global_load_dwordx4 v[120:123], v146, s[100:101] nt
	global_load_dwordx4 v[124:127], v147, s[100:101] nt
	ds_write_b128 v148, v[152:155] offset:32768
	ds_write_b128 v148, v[156:159] offset:32896
	ds_write_b128 v149, v[160:163] offset:32768
	ds_write_b128 v149, v[164:167] offset:32896
	s_waitcnt lgkmcnt(0)
	s_barrier
; #define G_SCHED __builtin_amdgcn_sched_barrier(0)
; #define CI_LOAD(R, kt) do { _Pragma("unroll") for (int _j = 0; _j < 16; ++_j) R[_j] = __builtin_nontemporal_load((const f32x4*)(src + (size_t)((kt) * 128 + _j) * LDB)); } while (0)
; template <int LDB>
; __device__ __forceinline__ void convert_image(const float* __restrict__ W, int col0, int col1, unsigned char* __restrict__ img, LAS3 char* lds, int wid) {
;     ...
;     f32x4 ra[16], rb[16];
;     CI_LOAD(ra, 0);
;     for (int kt = 0; kt < 16; kt += 2) {
;         CI_LOAD(rb, kt + 1); G_SCHED;
;         CI_CONV(ra, kt); G_SCHED;
;         CI_LOAD(ra, (kt + 2 < 16) ? kt + 2 : 15); G_SCHED;
;         CI_CONV(rb, kt + 1); G_SCHED;
;     }
	ds_read_b128 v[168:171], v150 offset:32768
	ds_read_b128 v[172:175], v150 offset:33792
	ds_read_b128 v[176:179], v150 offset:34816
	ds_read_b128 v[180:183], v150 offset:35840
	s_waitcnt lgkmcnt(3)
	global_store_dwordx4 v150, v[168:171], s[6:7] nt
	s_waitcnt lgkmcnt(2)
	global_store_dwordx4 v150, v[172:175], s[6:7] offset:1024 nt
	s_waitcnt lgkmcnt(1)
	global_store_dwordx4 v150, v[176:179], s[6:7] offset:2048 nt
	s_waitcnt lgkmcnt(0)
	global_store_dwordx4 v150, v[180:183], s[6:7] offset:3072 nt
	s_add_u32 s6, s6, 0x8000
	s_addc_u32 s7, s7, 0
	s_waitcnt vmcnt(44)
	v_cvt_scalef32_pk_fp8_f32 v152, v184, v188, s5
	v_cvt_scalef32_pk_fp8_f32 v156, v185, v189, s5
	v_cvt_scalef32_pk_fp8_f32 v160, v186, v190, s5
	v_cvt_scalef32_pk_fp8_f32 v164, v187, v191, s5
	v_cvt_scalef32_pk_fp8_f32 v153, v200, v204, s5
	v_cvt_scalef32_pk_fp8_f32 v157, v201, v205, s5
	v_cvt_scalef32_pk_fp8_f32 v161, v202, v206, s5
	v_cvt_scalef32_pk_fp8_f32 v165, v203, v207, s5
	v_cvt_scalef32_pk_fp8_f32 v154, v216, v220, s5
	v_cvt_scalef32_pk_fp8_f32 v158, v217, v221, s5
	v_cvt_scalef32_pk_fp8_f32 v162, v218, v222, s5
	v_cvt_scalef32_pk_fp8_f32 v166, v219, v223, s5
	v_cvt_scalef32_pk_fp8_f32 v155, v232, v236, s5
	v_cvt_scalef32_pk_fp8_f32 v159, v233, v237, s5
	v_cvt_scalef32_pk_fp8_f32 v163, v234, v238, s5
	v_cvt_scalef32_pk_fp8_f32 v167, v235, v239, s5
	v_cvt_scalef32_pk_fp8_f32 v152, v192, v196, s5 op_sel:[0,0,0,1]
	v_cvt_scalef32_pk_fp8_f32 v156, v193, v197, s5 op_sel:[0,0,0,1]
	v_cvt_scalef32_pk_fp8_f32 v160, v194, v198, s5 op_sel:[0,0,0,1]
	v_cvt_scalef32_pk_fp8_f32 v164, v195, v199, s5 op_sel:[0,0,0,1]
	v_cvt_scalef32_pk_fp8_f32 v153, v208, v212, s5 op_sel:[0,0,0,1]
	v_cvt_scalef32_pk_fp8_f32 v157, v209, v213, s5 op_sel:[0,0,0,1]
	v_cvt_scalef32_pk_fp8_f32 v161, v210, v214, s5 op_sel:[0,0,0,1]
	v_cvt_scalef32_pk_fp8_f32 v165, v211, v215, s5 op_sel:[0,0,0,1]
	v_cvt_scalef32_pk_fp8_f32 v154, v224, v228, s5 op_sel:[0,0,0,1]
	v_cvt_scalef32_pk_fp8_f32 v158, v225, v229, s5 op_sel:[0,0,0,1]
	v_cvt_scalef32_pk_fp8_f32 v162, v226, v230, s5 op_sel:[0,0,0,1]
	v_cvt_scalef32_pk_fp8_f32 v166, v227, v231, s5 op_sel:[0,0,0,1]
	v_cvt_scalef32_pk_fp8_f32 v155, v240, v244, s5 op_sel:[0,0,0,1]
	v_cvt_scalef32_pk_fp8_f32 v159, v241, v245, s5 op_sel:[0,0,0,1]
	v_cvt_scalef32_pk_fp8_f32 v163, v242, v246, s5 op_sel:[0,0,0,1]
	v_cvt_scalef32_pk_fp8_f32 v167, v243, v247, s5 op_sel:[0,0,0,1]
	s_add_u32 s100, s100, s88
	s_addc_u32 s101, s101, 0
	global_load_dwordx4 v[184:187], v132, s[100:101] nt
	global_load_dwordx4 v[188:191], v133, s[100:101] nt
	global_load_dwordx4 v[192:195], v134, s[100:101] nt
	global_load_dwordx4 v[196:199], v135, s[100:101] nt
	global_load_dwordx4 v[200:203], v136, s[100:101] nt
	global_load_dwordx4 v[204:207], v137, s[100:101] nt
	global_load_dwordx4 v[208:211], v138, s[100:101] nt
	global_load_dwordx4 v[212:215], v139, s[100:101] nt
	global_load_dwordx4 v[216:219], v140, s[100:101] nt
	global_load_dwordx4 v[220:223], v141, s[100:101] nt
	global_load_dwordx4 v[224:227], v142, s[100:101] nt
	global_load_dwordx4 v[228:231], v143, s[100:101] nt
	global_load_dwordx4 v[232:235], v144, s[100:101] nt
	global_load_dwordx4 v[236:239], v145, s[100:101] nt
	global_load_dwordx4 v[240:243], v146, s[100:101] nt
	global_load_dwordx4 v[244:247], v147, s[100:101] nt
	ds_write_b128 v148, v[152:155] offset:0
	ds_write_b128 v148, v[156:159] offset:128
	ds_write_b128 v149, v[160:163] offset:0
	ds_write_b128 v149, v[164:167] offset:128
	s_waitcnt lgkmcnt(0)
	s_barrier
	ds_read_b128 v[168:171], v150 offset:0
	ds_read_b128 v[172:175], v150 offset:1024
	ds_read_b128 v[176:179], v150 offset:2048
	ds_read_b128 v[180:183], v150 offset:3072
	s_waitcnt lgkmcnt(3)
	global_store_dwordx4 v150, v[168:171], s[6:7] nt
	s_waitcnt lgkmcnt(2)
	global_store_dwordx4 v150, v[172:175], s[6:7] offset:1024 nt
	s_waitcnt lgkmcnt(1)
	global_store_dwordx4 v150, v[176:179], s[6:7] offset:2048 nt
	s_waitcnt lgkmcnt(0)
	global_store_dwordx4 v150, v[180:183], s[6:7] offset:3072 nt
	s_add_u32 s6, s6, 0x8000
	s_addc_u32 s7, s7, 0
	s_waitcnt vmcnt(44)
	v_cvt_scalef32_pk_fp8_f32 v152, v0, v4, s5
	v_cvt_scalef32_pk_fp8_f32 v156, v1, v5, s5
	v_cvt_scalef32_pk_fp8_f32 v160, v2, v6, s5
	v_cvt_scalef32_pk_fp8_f32 v164, v3, v7, s5
	v_cvt_scalef32_pk_fp8_f32 v153, v16, v20, s5
	v_cvt_scalef32_pk_fp8_f32 v157, v17, v21, s5
	v_cvt_scalef32_pk_fp8_f32 v161, v18, v22, s5
	v_cvt_scalef32_pk_fp8_f32 v165, v19, v23, s5
	v_cvt_scalef32_pk_fp8_f32 v154, v32, v36, s5
	v_cvt_scalef32_pk_fp8_f32 v158, v33, v37, s5
	v_cvt_scalef32_pk_fp8_f32 v162, v34, v38, s5
	v_cvt_scalef32_pk_fp8_f32 v166, v35, v39, s5
	v_cvt_scalef32_pk_fp8_f32 v155, v48, v52, s5
	v_cvt_scalef32_pk_fp8_f32 v159, v49, v53, s5
	v_cvt_scalef32_pk_fp8_f32 v163, v50, v54, s5
	v_cvt_scalef32_pk_fp8_f32 v167, v51, v55, s5
	v_cvt_scalef32_pk_fp8_f32 v152, v8, v12, s5 op_sel:[0,0,0,1]
	v_cvt_scalef32_pk_fp8_f32 v156, v9, v13, s5 op_sel:[0,0,0,1]
	v_cvt_scalef32_pk_fp8_f32 v160, v10, v14, s5 op_sel:[0,0,0,1]
	v_cvt_scalef32_pk_fp8_f32 v164, v11, v15, s5 op_sel:[0,0,0,1]
	v_cvt_scalef32_pk_fp8_f32 v153, v24, v28, s5 op_sel:[0,0,0,1]
	v_cvt_scalef32_pk_fp8_f32 v157, v25, v29, s5 op_sel:[0,0,0,1]
	v_cvt_scalef32_pk_fp8_f32 v161, v26, v30, s5 op_sel:[0,0,0,1]
	v_cvt_scalef32_pk_fp8_f32 v165, v27, v31, s5 op_sel:[0,0,0,1]
	v_cvt_scalef32_pk_fp8_f32 v154, v40, v44, s5 op_sel:[0,0,0,1]
	v_cvt_scalef32_pk_fp8_f32 v158, v41, v45, s5 op_sel:[0,0,0,1]
	v_cvt_scalef32_pk_fp8_f32 v162, v42, v46, s5 op_sel:[0,0,0,1]
	v_cvt_scalef32_pk_fp8_f32 v166, v43, v47, s5 op_sel:[0,0,0,1]
	v_cvt_scalef32_pk_fp8_f32 v155, v56, v60, s5 op_sel:[0,0,0,1]
	v_cvt_scalef32_pk_fp8_f32 v159, v57, v61, s5 op_sel:[0,0,0,1]
	v_cvt_scalef32_pk_fp8_f32 v163, v58, v62, s5 op_sel:[0,0,0,1]
	v_cvt_scalef32_pk_fp8_f32 v167, v59, v63, s5 op_sel:[0,0,0,1]
	s_add_u32 s100, s100, s88
	s_addc_u32 s101, s101, 0
	global_load_dwordx4 v[0:3], v132, s[100:101] nt
	global_load_dwordx4 v[4:7], v133, s[100:101] nt
	global_load_dwordx4 v[8:11], v134, s[100:101] nt
	global_load_dwordx4 v[12:15], v135, s[100:101] nt
	global_load_dwordx4 v[16:19], v136, s[100:101] nt
	global_load_dwordx4 v[20:23], v137, s[100:101] nt
	global_load_dwordx4 v[24:27], v138, s[100:101] nt
	global_load_dwordx4 v[28:31], v139, s[100:101] nt
	global_load_dwordx4 v[32:35], v140, s[100:101] nt
	global_load_dwordx4 v[36:39], v141, s[100:101] nt
	global_load_dwordx4 v[40:43], v142, s[100:101] nt
	global_load_dwordx4 v[44:47], v143, s[100:101] nt
	global_load_dwordx4 v[48:51], v144, s[100:101] nt
	global_load_dwordx4 v[52:55], v145, s[100:101] nt
	global_load_dwordx4 v[56:59], v146, s[100:101] nt
	global_load_dwordx4 v[60:63], v147, s[100:101] nt
	ds_write_b128 v148, v[152:155] offset:32768
	ds_write_b128 v148, v[156:159] offset:32896
	ds_write_b128 v149, v[160:163] offset:32768
	ds_write_b128 v149, v[164:167] offset:32896
	s_waitcnt lgkmcnt(0)
	s_barrier
; #define G_SCHED __builtin_amdgcn_sched_barrier(0)
; #define CI_LOAD(R, kt) do { _Pragma("unroll") for (int _j = 0; _j < 16; ++_j) R[_j] = __builtin_nontemporal_load((const f32x4*)(src + (size_t)((kt) * 128 + _j) * LDB)); } while (0)
; template <int LDB>
; __device__ __forceinline__ void convert_image(const float* __restrict__ W, int col0, int col1, unsigned char* __restrict__ img, LAS3 char* lds, int wid) {
;     ...
;     f32x4 ra[16], rb[16];
;     CI_LOAD(ra, 0);
;     for (int kt = 0; kt < 16; kt += 2) {
;         CI_LOAD(rb, kt + 1); G_SCHED;
;         CI_CONV(ra, kt); G_SCHED;
;         CI_LOAD(ra, (kt + 2 < 16) ? kt + 2 : 15); G_SCHED;
;         CI_CONV(rb, kt + 1); G_SCHED;
;     }
	ds_read_b128 v[168:171], v150 offset:32768
	ds_read_b128 v[172:175], v150 offset:33792
	ds_read_b128 v[176:179], v150 offset:34816
	ds_read_b128 v[180:183], v150 offset:35840
	s_waitcnt lgkmcnt(3)
	global_store_dwordx4 v150, v[168:171], s[6:7] nt
	s_waitcnt lgkmcnt(2)
	global_store_dwordx4 v150, v[172:175], s[6:7] offset:1024 nt
	s_waitcnt lgkmcnt(1)
	global_store_dwordx4 v150, v[176:179], s[6:7] offset:2048 nt
	s_waitcnt lgkmcnt(0)
	global_store_dwordx4 v150, v[180:183], s[6:7] offset:3072 nt
	s_add_u32 s6, s6, 0x8000
	s_addc_u32 s7, s7, 0
	s_waitcnt vmcnt(44)
	v_cvt_scalef32_pk_fp8_f32 v152, v64, v68, s5
	v_cvt_scalef32_pk_fp8_f32 v156, v65, v69, s5
	v_cvt_scalef32_pk_fp8_f32 v160, v66, v70, s5
	v_cvt_scalef32_pk_fp8_f32 v164, v67, v71, s5
	v_cvt_scalef32_pk_fp8_f32 v153, v80, v84, s5
	v_cvt_scalef32_pk_fp8_f32 v157, v81, v85, s5
	v_cvt_scalef32_pk_fp8_f32 v161, v82, v86, s5
	v_cvt_scalef32_pk_fp8_f32 v165, v83, v87, s5
	v_cvt_scalef32_pk_fp8_f32 v154, v96, v100, s5
	v_cvt_scalef32_pk_fp8_f32 v158, v97, v101, s5
	v_cvt_scalef32_pk_fp8_f32 v162, v98, v102, s5
	v_cvt_scalef32_pk_fp8_f32 v166, v99, v103, s5
	v_cvt_scalef32_pk_fp8_f32 v155, v112, v116, s5
	v_cvt_scalef32_pk_fp8_f32 v159, v113, v117, s5
	v_cvt_scalef32_pk_fp8_f32 v163, v114, v118, s5
	v_cvt_scalef32_pk_fp8_f32 v167, v115, v119, s5
	v_cvt_scalef32_pk_fp8_f32 v152, v72, v76, s5 op_sel:[0,0,0,1]
	v_cvt_scalef32_pk_fp8_f32 v156, v73, v77, s5 op_sel:[0,0,0,1]
	v_cvt_scalef32_pk_fp8_f32 v160, v74, v78, s5 op_sel:[0,0,0,1]
	v_cvt_scalef32_pk_fp8_f32 v164, v75, v79, s5 op_sel:[0,0,0,1]
	v_cvt_scalef32_pk_fp8_f32 v153, v88, v92, s5 op_sel:[0,0,0,1]
	v_cvt_scalef32_pk_fp8_f32 v157, v89, v93, s5 op_sel:[0,0,0,1]
	v_cvt_scalef32_pk_fp8_f32 v161, v90, v94, s5 op_sel:[0,0,0,1]
	v_cvt_scalef32_pk_fp8_f32 v165, v91, v95, s5 op_sel:[0,0,0,1]
	v_cvt_scalef32_pk_fp8_f32 v154, v104, v108, s5 op_sel:[0,0,0,1]
	v_cvt_scalef32_pk_fp8_f32 v158, v105, v109, s5 op_sel:[0,0,0,1]
	v_cvt_scalef32_pk_fp8_f32 v162, v106, v110, s5 op_sel:[0,0,0,1]
	v_cvt_scalef32_pk_fp8_f32 v166, v107, v111, s5 op_sel:[0,0,0,1]
	v_cvt_scalef32_pk_fp8_f32 v155, v120, v124, s5 op_sel:[0,0,0,1]
	v_cvt_scalef32_pk_fp8_f32 v159, v121, v125, s5 op_sel:[0,0,0,1]
	v_cvt_scalef32_pk_fp8_f32 v163, v122, v126, s5 op_sel:[0,0,0,1]
	v_cvt_scalef32_pk_fp8_f32 v167, v123, v127, s5 op_sel:[0,0,0,1]
	s_add_u32 s100, s100, s88
	s_addc_u32 s101, s101, 0
	global_load_dwordx4 v[64:67], v132, s[100:101] nt
	global_load_dwordx4 v[68:71], v133, s[100:101] nt
	global_load_dwordx4 v[72:75], v134, s[100:101] nt
	global_load_dwordx4 v[76:79], v135, s[100:101] nt
	global_load_dwordx4 v[80:83], v136, s[100:101] nt
	global_load_dwordx4 v[84:87], v137, s[100:101] nt
	global_load_dwordx4 v[88:91], v138, s[100:101] nt
	global_load_dwordx4 v[92:95], v139, s[100:101] nt
	global_load_dwordx4 v[96:99], v140, s[100:101] nt
	global_load_dwordx4 v[100:103], v141, s[100:101] nt
	global_load_dwordx4 v[104:107], v142, s[100:101] nt
	global_load_dwordx4 v[108:111], v143, s[100:101] nt
	global_load_dwordx4 v[112:115], v144, s[100:101] nt
	global_load_dwordx4 v[116:119], v145, s[100:101] nt
	global_load_dwordx4 v[120:123], v146, s[100:101] nt
	global_load_dwordx4 v[124:127], v147, s[100:101] nt
	ds_write_b128 v148, v[152:155] offset:0
	ds_write_b128 v148, v[156:159] offset:128
	ds_write_b128 v149, v[160:163] offset:0
	ds_write_b128 v149, v[164:167] offset:128
	s_waitcnt lgkmcnt(0)
	s_barrier
	ds_read_b128 v[168:171], v150 offset:0
	ds_read_b128 v[172:175], v150 offset:1024
	ds_read_b128 v[176:179], v150 offset:2048
	ds_read_b128 v[180:183], v150 offset:3072
	s_waitcnt lgkmcnt(3)
	global_store_dwordx4 v150, v[168:171], s[6:7] nt
	s_waitcnt lgkmcnt(2)
	global_store_dwordx4 v150, v[172:175], s[6:7] offset:1024 nt
	s_waitcnt lgkmcnt(1)
	global_store_dwordx4 v150, v[176:179], s[6:7] offset:2048 nt
	s_waitcnt lgkmcnt(0)
	global_store_dwordx4 v150, v[180:183], s[6:7] offset:3072 nt
	s_add_u32 s6, s6, 0x8000
	s_addc_u32 s7, s7, 0
	s_waitcnt vmcnt(44)
	v_cvt_scalef32_pk_fp8_f32 v152, v184, v188, s5
	v_cvt_scalef32_pk_fp8_f32 v156, v185, v189, s5
	v_cvt_scalef32_pk_fp8_f32 v160, v186, v190, s5
	v_cvt_scalef32_pk_fp8_f32 v164, v187, v191, s5
	v_cvt_scalef32_pk_fp8_f32 v153, v200, v204, s5
	v_cvt_scalef32_pk_fp8_f32 v157, v201, v205, s5
	v_cvt_scalef32_pk_fp8_f32 v161, v202, v206, s5
	v_cvt_scalef32_pk_fp8_f32 v165, v203, v207, s5
	v_cvt_scalef32_pk_fp8_f32 v154, v216, v220, s5
	v_cvt_scalef32_pk_fp8_f32 v158, v217, v221, s5
	v_cvt_scalef32_pk_fp8_f32 v162, v218, v222, s5
	v_cvt_scalef32_pk_fp8_f32 v166, v219, v223, s5
	v_cvt_scalef32_pk_fp8_f32 v155, v232, v236, s5
	v_cvt_scalef32_pk_fp8_f32 v159, v233, v237, s5
	v_cvt_scalef32_pk_fp8_f32 v163, v234, v238, s5
	v_cvt_scalef32_pk_fp8_f32 v167, v235, v239, s5
	v_cvt_scalef32_pk_fp8_f32 v152, v192, v196, s5 op_sel:[0,0,0,1]
	v_cvt_scalef32_pk_fp8_f32 v156, v193, v197, s5 op_sel:[0,0,0,1]
	v_cvt_scalef32_pk_fp8_f32 v160, v194, v198, s5 op_sel:[0,0,0,1]
	v_cvt_scalef32_pk_fp8_f32 v164, v195, v199, s5 op_sel:[0,0,0,1]
	v_cvt_scalef32_pk_fp8_f32 v153, v208, v212, s5 op_sel:[0,0,0,1]
	v_cvt_scalef32_pk_fp8_f32 v157, v209, v213, s5 op_sel:[0,0,0,1]
	v_cvt_scalef32_pk_fp8_f32 v161, v210, v214, s5 op_sel:[0,0,0,1]
	v_cvt_scalef32_pk_fp8_f32 v165, v211, v215, s5 op_sel:[0,0,0,1]
	v_cvt_scalef32_pk_fp8_f32 v154, v224, v228, s5 op_sel:[0,0,0,1]
	v_cvt_scalef32_pk_fp8_f32 v158, v225, v229, s5 op_sel:[0,0,0,1]
	v_cvt_scalef32_pk_fp8_f32 v162, v226, v230, s5 op_sel:[0,0,0,1]
	v_cvt_scalef32_pk_fp8_f32 v166, v227, v231, s5 op_sel:[0,0,0,1]
	v_cvt_scalef32_pk_fp8_f32 v155, v240, v244, s5 op_sel:[0,0,0,1]
	v_cvt_scalef32_pk_fp8_f32 v159, v241, v245, s5 op_sel:[0,0,0,1]
	v_cvt_scalef32_pk_fp8_f32 v163, v242, v246, s5 op_sel:[0,0,0,1]
	v_cvt_scalef32_pk_fp8_f32 v167, v243, v247, s5 op_sel:[0,0,0,1]
	s_add_u32 s100, s100, s88
	s_addc_u32 s101, s101, 0
	global_load_dwordx4 v[184:187], v132, s[100:101] nt
	global_load_dwordx4 v[188:191], v133, s[100:101] nt
	global_load_dwordx4 v[192:195], v134, s[100:101] nt
	global_load_dwordx4 v[196:199], v135, s[100:101] nt
	global_load_dwordx4 v[200:203], v136, s[100:101] nt
	global_load_dwordx4 v[204:207], v137, s[100:101] nt
	global_load_dwordx4 v[208:211], v138, s[100:101] nt
	global_load_dwordx4 v[212:215], v139, s[100:101] nt
	global_load_dwordx4 v[216:219], v140, s[100:101] nt
	global_load_dwordx4 v[220:223], v141, s[100:101] nt
	global_load_dwordx4 v[224:227], v142, s[100:101] nt
	global_load_dwordx4 v[228:231], v143, s[100:101] nt
	global_load_dwordx4 v[232:235], v144, s[100:101] nt
	global_load_dwordx4 v[236:239], v145, s[100:101] nt
	global_load_dwordx4 v[240:243], v146, s[100:101] nt
	global_load_dwordx4 v[244:247], v147, s[100:101] nt
	ds_write_b128 v148, v[152:155] offset:32768
	ds_write_b128 v148, v[156:159] offset:32896
	ds_write_b128 v149, v[160:163] offset:32768
	ds_write_b128 v149, v[164:167] offset:32896
	s_waitcnt lgkmcnt(0)
	s_barrier
; #define G_SCHED __builtin_amdgcn_sched_barrier(0)
; #define CI_LOAD(R, kt) do { _Pragma("unroll") for (int _j = 0; _j < 16; ++_j) R[_j] = __builtin_nontemporal_load((const f32x4*)(src + (size_t)((kt) * 128 + _j) * LDB)); } while (0)
; template <int LDB>
; __device__ __forceinline__ void convert_image(const float* __restrict__ W, int col0, int col1, unsigned char* __restrict__ img, LAS3 char* lds, int wid) {
;     ...
;     f32x4 ra[16], rb[16];
;     CI_LOAD(ra, 0);
;     for (int kt = 0; kt < 16; kt += 2) {
;         CI_LOAD(rb, kt + 1); G_SCHED;
;         CI_CONV(ra, kt); G_SCHED;
;         CI_LOAD(ra, (kt + 2 < 16) ? kt + 2 : 15); G_SCHED;
;         CI_CONV(rb, kt + 1); G_SCHED;
;     }
	ds_read_b128 v[168:171], v150 offset:32768
	ds_read_b128 v[172:175], v150 offset:33792
	ds_read_b128 v[176:179], v150 offset:34816
	ds_read_b128 v[180:183], v150 offset:35840
	s_waitcnt lgkmcnt(3)
	global_store_dwordx4 v150, v[168:171], s[6:7] nt
	s_waitcnt lgkmcnt(2)
	global_store_dwordx4 v150, v[172:175], s[6:7] offset:1024 nt
	s_waitcnt lgkmcnt(1)
	global_store_dwordx4 v150, v[176:179], s[6:7] offset:2048 nt
	s_waitcnt lgkmcnt(0)
	global_store_dwordx4 v150, v[180:183], s[6:7] offset:3072 nt
	s_add_u32 s6, s6, 0x8000
	s_addc_u32 s7, s7, 0
	s_waitcnt vmcnt(44)
	v_cvt_scalef32_pk_fp8_f32 v152, v0, v4, s5
	v_cvt_scalef32_pk_fp8_f32 v156, v1, v5, s5
	v_cvt_scalef32_pk_fp8_f32 v160, v2, v6, s5
	v_cvt_scalef32_pk_fp8_f32 v164, v3, v7, s5
	v_cvt_scalef32_pk_fp8_f32 v153, v16, v20, s5
	v_cvt_scalef32_pk_fp8_f32 v157, v17, v21, s5
	v_cvt_scalef32_pk_fp8_f32 v161, v18, v22, s5
	v_cvt_scalef32_pk_fp8_f32 v165, v19, v23, s5
	v_cvt_scalef32_pk_fp8_f32 v154, v32, v36, s5
	v_cvt_scalef32_pk_fp8_f32 v158, v33, v37, s5
	v_cvt_scalef32_pk_fp8_f32 v162, v34, v38, s5
	v_cvt_scalef32_pk_fp8_f32 v166, v35, v39, s5
	v_cvt_scalef32_pk_fp8_f32 v155, v48, v52, s5
	v_cvt_scalef32_pk_fp8_f32 v159, v49, v53, s5
	v_cvt_scalef32_pk_fp8_f32 v163, v50, v54, s5
	v_cvt_scalef32_pk_fp8_f32 v167, v51, v55, s5
	v_cvt_scalef32_pk_fp8_f32 v152, v8, v12, s5 op_sel:[0,0,0,1]
	v_cvt_scalef32_pk_fp8_f32 v156, v9, v13, s5 op_sel:[0,0,0,1]
	v_cvt_scalef32_pk_fp8_f32 v160, v10, v14, s5 op_sel:[0,0,0,1]
	v_cvt_scalef32_pk_fp8_f32 v164, v11, v15, s5 op_sel:[0,0,0,1]
	v_cvt_scalef32_pk_fp8_f32 v153, v24, v28, s5 op_sel:[0,0,0,1]
	v_cvt_scalef32_pk_fp8_f32 v157, v25, v29, s5 op_sel:[0,0,0,1]
	v_cvt_scalef32_pk_fp8_f32 v161, v26, v30, s5 op_sel:[0,0,0,1]
	v_cvt_scalef32_pk_fp8_f32 v165, v27, v31, s5 op_sel:[0,0,0,1]
	v_cvt_scalef32_pk_fp8_f32 v154, v40, v44, s5 op_sel:[0,0,0,1]
	v_cvt_scalef32_pk_fp8_f32 v158, v41, v45, s5 op_sel:[0,0,0,1]
	v_cvt_scalef32_pk_fp8_f32 v162, v42, v46, s5 op_sel:[0,0,0,1]
	v_cvt_scalef32_pk_fp8_f32 v166, v43, v47, s5 op_sel:[0,0,0,1]
	v_cvt_scalef32_pk_fp8_f32 v155, v56, v60, s5 op_sel:[0,0,0,1]
	v_cvt_scalef32_pk_fp8_f32 v159, v57, v61, s5 op_sel:[0,0,0,1]
	v_cvt_scalef32_pk_fp8_f32 v163, v58, v62, s5 op_sel:[0,0,0,1]
	v_cvt_scalef32_pk_fp8_f32 v167, v59, v63, s5 op_sel:[0,0,0,1]
	s_add_u32 s100, s100, s88
	s_addc_u32 s101, s101, 0
	global_load_dwordx4 v[0:3], v132, s[100:101] nt
	global_load_dwordx4 v[4:7], v133, s[100:101] nt
	global_load_dwordx4 v[8:11], v134, s[100:101] nt
	global_load_dwordx4 v[12:15], v135, s[100:101] nt
	global_load_dwordx4 v[16:19], v136, s[100:101] nt
	global_load_dwordx4 v[20:23], v137, s[100:101] nt
	global_load_dwordx4 v[24:27], v138, s[100:101] nt
	global_load_dwordx4 v[28:31], v139, s[100:101] nt
	global_load_dwordx4 v[32:35], v140, s[100:101] nt
	global_load_dwordx4 v[36:39], v141, s[100:101] nt
	global_load_dwordx4 v[40:43], v142, s[100:101] nt
	global_load_dwordx4 v[44:47], v143, s[100:101] nt
	global_load_dwordx4 v[48:51], v144, s[100:101] nt
	global_load_dwordx4 v[52:55], v145, s[100:101] nt
	global_load_dwordx4 v[56:59], v146, s[100:101] nt
	global_load_dwordx4 v[60:63], v147, s[100:101] nt
	ds_write_b128 v148, v[152:155] offset:0
	ds_write_b128 v148, v[156:159] offset:128
	ds_write_b128 v149, v[160:163] offset:0
	ds_write_b128 v149, v[164:167] offset:128
	s_waitcnt lgkmcnt(0)
	s_barrier
	ds_read_b128 v[168:171], v150 offset:0
	ds_read_b128 v[172:175], v150 offset:1024
	ds_read_b128 v[176:179], v150 offset:2048
	ds_read_b128 v[180:183], v150 offset:3072
	s_waitcnt lgkmcnt(3)
	global_store_dwordx4 v150, v[168:171], s[6:7] nt
	s_waitcnt lgkmcnt(2)
	global_store_dwordx4 v150, v[172:175], s[6:7] offset:1024 nt
	s_waitcnt lgkmcnt(1)
	global_store_dwordx4 v150, v[176:179], s[6:7] offset:2048 nt
	s_waitcnt lgkmcnt(0)
	global_store_dwordx4 v150, v[180:183], s[6:7] offset:3072 nt
	s_add_u32 s6, s6, 0x8000
	s_addc_u32 s7, s7, 0
	s_waitcnt vmcnt(44)
	v_cvt_scalef32_pk_fp8_f32 v152, v64, v68, s5
	v_cvt_scalef32_pk_fp8_f32 v156, v65, v69, s5
	v_cvt_scalef32_pk_fp8_f32 v160, v66, v70, s5
	v_cvt_scalef32_pk_fp8_f32 v164, v67, v71, s5
	v_cvt_scalef32_pk_fp8_f32 v153, v80, v84, s5
	v_cvt_scalef32_pk_fp8_f32 v157, v81, v85, s5
	v_cvt_scalef32_pk_fp8_f32 v161, v82, v86, s5
	v_cvt_scalef32_pk_fp8_f32 v165, v83, v87, s5
	v_cvt_scalef32_pk_fp8_f32 v154, v96, v100, s5
	v_cvt_scalef32_pk_fp8_f32 v158, v97, v101, s5
	v_cvt_scalef32_pk_fp8_f32 v162, v98, v102, s5
	v_cvt_scalef32_pk_fp8_f32 v166, v99, v103, s5
	v_cvt_scalef32_pk_fp8_f32 v155, v112, v116, s5
	v_cvt_scalef32_pk_fp8_f32 v159, v113, v117, s5
	v_cvt_scalef32_pk_fp8_f32 v163, v114, v118, s5
	v_cvt_scalef32_pk_fp8_f32 v167, v115, v119, s5
	v_cvt_scalef32_pk_fp8_f32 v152, v72, v76, s5 op_sel:[0,0,0,1]
	v_cvt_scalef32_pk_fp8_f32 v156, v73, v77, s5 op_sel:[0,0,0,1]
	v_cvt_scalef32_pk_fp8_f32 v160, v74, v78, s5 op_sel:[0,0,0,1]
	v_cvt_scalef32_pk_fp8_f32 v164, v75, v79, s5 op_sel:[0,0,0,1]
	v_cvt_scalef32_pk_fp8_f32 v153, v88, v92, s5 op_sel:[0,0,0,1]
	v_cvt_scalef32_pk_fp8_f32 v157, v89, v93, s5 op_sel:[0,0,0,1]
	v_cvt_scalef32_pk_fp8_f32 v161, v90, v94, s5 op_sel:[0,0,0,1]
	v_cvt_scalef32_pk_fp8_f32 v165, v91, v95, s5 op_sel:[0,0,0,1]
	v_cvt_scalef32_pk_fp8_f32 v154, v104, v108, s5 op_sel:[0,0,0,1]
	v_cvt_scalef32_pk_fp8_f32 v158, v105, v109, s5 op_sel:[0,0,0,1]
	v_cvt_scalef32_pk_fp8_f32 v162, v106, v110, s5 op_sel:[0,0,0,1]
	v_cvt_scalef32_pk_fp8_f32 v166, v107, v111, s5 op_sel:[0,0,0,1]
	v_cvt_scalef32_pk_fp8_f32 v155, v120, v124, s5 op_sel:[0,0,0,1]
	v_cvt_scalef32_pk_fp8_f32 v159, v121, v125, s5 op_sel:[0,0,0,1]
	v_cvt_scalef32_pk_fp8_f32 v163, v122, v126, s5 op_sel:[0,0,0,1]
	v_cvt_scalef32_pk_fp8_f32 v167, v123, v127, s5 op_sel:[0,0,0,1]
	ds_write_b128 v148, v[152:155] offset:32768
	ds_write_b128 v148, v[156:159] offset:32896
	ds_write_b128 v149, v[160:163] offset:32768
	ds_write_b128 v149, v[164:167] offset:32896
	s_waitcnt lgkmcnt(0)
	s_barrier
; #define G_SCHED __builtin_amdgcn_sched_barrier(0)
; #define CI_LOAD(R, kt) do { _Pragma("unroll") for (int _j = 0; _j < 16; ++_j) R[_j] = __builtin_nontemporal_load((const f32x4*)(src + (size_t)((kt) * 128 + _j) * LDB)); } while (0)
; template <int LDB>
; __device__ __forceinline__ void convert_image(const float* __restrict__ W, int col0, int col1, unsigned char* __restrict__ img, LAS3 char* lds, int wid) {
;     ...
;     f32x4 ra[16], rb[16];
;     CI_LOAD(ra, 0);
;     for (int kt = 0; kt < 16; kt += 2) {
;         CI_LOAD(rb, kt + 1); G_SCHED;
;         CI_CONV(ra, kt); G_SCHED;
;         CI_LOAD(ra, (kt + 2 < 16) ? kt + 2 : 15); G_SCHED;
;         CI_CONV(rb, kt + 1); G_SCHED;
;     }
;     asm volatile("s_waitcnt vmcnt(0)" ::: "memory");
;     __syncthreads();
	ds_read_b128 v[168:171], v150 offset:32768
	ds_read_b128 v[172:175], v150 offset:33792
	ds_read_b128 v[176:179], v150 offset:34816
	ds_read_b128 v[180:183], v150 offset:35840
	s_waitcnt lgkmcnt(3)
	global_store_dwordx4 v150, v[168:171], s[6:7] nt
	s_waitcnt lgkmcnt(2)
	global_store_dwordx4 v150, v[172:175], s[6:7] offset:1024 nt
	s_waitcnt lgkmcnt(1)
	global_store_dwordx4 v150, v[176:179], s[6:7] offset:2048 nt
	s_waitcnt lgkmcnt(0)
	global_store_dwordx4 v150, v[180:183], s[6:7] offset:3072 nt
	s_add_u32 s6, s6, 0x8000
	s_addc_u32 s7, s7, 0
	s_waitcnt vmcnt(28)
	v_cvt_scalef32_pk_fp8_f32 v152, v184, v188, s5
	v_cvt_scalef32_pk_fp8_f32 v156, v185, v189, s5
	v_cvt_scalef32_pk_fp8_f32 v160, v186, v190, s5
	v_cvt_scalef32_pk_fp8_f32 v164, v187, v191, s5
	v_cvt_scalef32_pk_fp8_f32 v153, v200, v204, s5
	v_cvt_scalef32_pk_fp8_f32 v157, v201, v205, s5
	v_cvt_scalef32_pk_fp8_f32 v161, v202, v206, s5
	v_cvt_scalef32_pk_fp8_f32 v165, v203, v207, s5
	v_cvt_scalef32_pk_fp8_f32 v154, v216, v220, s5
	v_cvt_scalef32_pk_fp8_f32 v158, v217, v221, s5
	v_cvt_scalef32_pk_fp8_f32 v162, v218, v222, s5
	v_cvt_scalef32_pk_fp8_f32 v166, v219, v223, s5
	v_cvt_scalef32_pk_fp8_f32 v155, v232, v236, s5
	v_cvt_scalef32_pk_fp8_f32 v159, v233, v237, s5
	v_cvt_scalef32_pk_fp8_f32 v163, v234, v238, s5
	v_cvt_scalef32_pk_fp8_f32 v167, v235, v239, s5
	v_cvt_scalef32_pk_fp8_f32 v152, v192, v196, s5 op_sel:[0,0,0,1]
	v_cvt_scalef32_pk_fp8_f32 v156, v193, v197, s5 op_sel:[0,0,0,1]
	v_cvt_scalef32_pk_fp8_f32 v160, v194, v198, s5 op_sel:[0,0,0,1]
	v_cvt_scalef32_pk_fp8_f32 v164, v195, v199, s5 op_sel:[0,0,0,1]
	v_cvt_scalef32_pk_fp8_f32 v153, v208, v212, s5 op_sel:[0,0,0,1]
	v_cvt_scalef32_pk_fp8_f32 v157, v209, v213, s5 op_sel:[0,0,0,1]
	v_cvt_scalef32_pk_fp8_f32 v161, v210, v214, s5 op_sel:[0,0,0,1]
	v_cvt_scalef32_pk_fp8_f32 v165, v211, v215, s5 op_sel:[0,0,0,1]
	v_cvt_scalef32_pk_fp8_f32 v154, v224, v228, s5 op_sel:[0,0,0,1]
	v_cvt_scalef32_pk_fp8_f32 v158, v225, v229, s5 op_sel:[0,0,0,1]
	v_cvt_scalef32_pk_fp8_f32 v162, v226, v230, s5 op_sel:[0,0,0,1]
	v_cvt_scalef32_pk_fp8_f32 v166, v227, v231, s5 op_sel:[0,0,0,1]
	v_cvt_scalef32_pk_fp8_f32 v155, v240, v244, s5 op_sel:[0,0,0,1]
	v_cvt_scalef32_pk_fp8_f32 v159, v241, v245, s5 op_sel:[0,0,0,1]
	v_cvt_scalef32_pk_fp8_f32 v163, v242, v246, s5 op_sel:[0,0,0,1]
	v_cvt_scalef32_pk_fp8_f32 v167, v243, v247, s5 op_sel:[0,0,0,1]
	ds_write_b128 v148, v[152:155] offset:0
	ds_write_b128 v148, v[156:159] offset:128
	ds_write_b128 v149, v[160:163] offset:0
	ds_write_b128 v149, v[164:167] offset:128
	s_waitcnt lgkmcnt(0)
	s_barrier
	ds_read_b128 v[168:171], v150 offset:0
	ds_read_b128 v[172:175], v150 offset:1024
	ds_read_b128 v[176:179], v150 offset:2048
	ds_read_b128 v[180:183], v150 offset:3072
	s_waitcnt lgkmcnt(3)
	global_store_dwordx4 v150, v[168:171], s[6:7] nt
	s_waitcnt lgkmcnt(2)
	global_store_dwordx4 v150, v[172:175], s[6:7] offset:1024 nt
	s_waitcnt lgkmcnt(1)
	global_store_dwordx4 v150, v[176:179], s[6:7] offset:2048 nt
	s_waitcnt lgkmcnt(0)
	global_store_dwordx4 v150, v[180:183], s[6:7] offset:3072 nt
	s_add_u32 s6, s6, 0x8000
	s_addc_u32 s7, s7, 0
	s_waitcnt vmcnt(12)
	v_cvt_scalef32_pk_fp8_f32 v152, v0, v4, s5
	v_cvt_scalef32_pk_fp8_f32 v156, v1, v5, s5
	v_cvt_scalef32_pk_fp8_f32 v160, v2, v6, s5
	v_cvt_scalef32_pk_fp8_f32 v164, v3, v7, s5
	v_cvt_scalef32_pk_fp8_f32 v153, v16, v20, s5
	v_cvt_scalef32_pk_fp8_f32 v157, v17, v21, s5
	v_cvt_scalef32_pk_fp8_f32 v161, v18, v22, s5
	v_cvt_scalef32_pk_fp8_f32 v165, v19, v23, s5
	v_cvt_scalef32_pk_fp8_f32 v154, v32, v36, s5
	v_cvt_scalef32_pk_fp8_f32 v158, v33, v37, s5
	v_cvt_scalef32_pk_fp8_f32 v162, v34, v38, s5
	v_cvt_scalef32_pk_fp8_f32 v166, v35, v39, s5
	v_cvt_scalef32_pk_fp8_f32 v155, v48, v52, s5
	v_cvt_scalef32_pk_fp8_f32 v159, v49, v53, s5
	v_cvt_scalef32_pk_fp8_f32 v163, v50, v54, s5
	v_cvt_scalef32_pk_fp8_f32 v167, v51, v55, s5
	v_cvt_scalef32_pk_fp8_f32 v152, v8, v12, s5 op_sel:[0,0,0,1]
	v_cvt_scalef32_pk_fp8_f32 v156, v9, v13, s5 op_sel:[0,0,0,1]
	v_cvt_scalef32_pk_fp8_f32 v160, v10, v14, s5 op_sel:[0,0,0,1]
	v_cvt_scalef32_pk_fp8_f32 v164, v11, v15, s5 op_sel:[0,0,0,1]
	v_cvt_scalef32_pk_fp8_f32 v153, v24, v28, s5 op_sel:[0,0,0,1]
	v_cvt_scalef32_pk_fp8_f32 v157, v25, v29, s5 op_sel:[0,0,0,1]
	v_cvt_scalef32_pk_fp8_f32 v161, v26, v30, s5 op_sel:[0,0,0,1]
	v_cvt_scalef32_pk_fp8_f32 v165, v27, v31, s5 op_sel:[0,0,0,1]
	v_cvt_scalef32_pk_fp8_f32 v154, v40, v44, s5 op_sel:[0,0,0,1]
	v_cvt_scalef32_pk_fp8_f32 v158, v41, v45, s5 op_sel:[0,0,0,1]
	v_cvt_scalef32_pk_fp8_f32 v162, v42, v46, s5 op_sel:[0,0,0,1]
	v_cvt_scalef32_pk_fp8_f32 v166, v43, v47, s5 op_sel:[0,0,0,1]
	v_cvt_scalef32_pk_fp8_f32 v155, v56, v60, s5 op_sel:[0,0,0,1]
	v_cvt_scalef32_pk_fp8_f32 v159, v57, v61, s5 op_sel:[0,0,0,1]
	v_cvt_scalef32_pk_fp8_f32 v163, v58, v62, s5 op_sel:[0,0,0,1]
	v_cvt_scalef32_pk_fp8_f32 v167, v59, v63, s5 op_sel:[0,0,0,1]
	ds_write_b128 v148, v[152:155] offset:32768
	ds_write_b128 v148, v[156:159] offset:32896
	ds_write_b128 v149, v[160:163] offset:32768
	ds_write_b128 v149, v[164:167] offset:32896
	s_waitcnt lgkmcnt(0)
	s_barrier
	ds_read_b128 v[168:171], v150 offset:32768
	ds_read_b128 v[172:175], v150 offset:33792
	ds_read_b128 v[176:179], v150 offset:34816
	ds_read_b128 v[180:183], v150 offset:35840
	s_waitcnt lgkmcnt(3)
	global_store_dwordx4 v150, v[168:171], s[6:7] nt
	s_waitcnt lgkmcnt(2)
	global_store_dwordx4 v150, v[172:175], s[6:7] offset:1024 nt
	s_waitcnt lgkmcnt(1)
	global_store_dwordx4 v150, v[176:179], s[6:7] offset:2048 nt
	s_waitcnt lgkmcnt(0)
	global_store_dwordx4 v150, v[180:183], s[6:7] offset:3072 nt
	s_add_u32 s6, s6, 0x8000
	s_addc_u32 s7, s7, 0
	s_waitcnt vmcnt(0)
	s_barrier
	s_cmp_lg_u32 vcc_hi, 0
	s_cbranch_scc1 .Lpc_skip
	v_mov_b32_e32 v152, 0
	v_mov_b32_e32 v153, 1
	v_cmp_eq_u32_e32 vcc, 0, v131
	s_and_saveexec_b64 s[4:5], vcc
	global_store_dword v152, v153, s[0:1] sc1
	s_mov_b64 exec, s[4:5]

; #define G_WAIT_V(n) asm volatile("s_waitcnt vmcnt(" #n ")" ::: "memory")
; #define G_BAR do { asm volatile("" ::: "memory"); __builtin_amdgcn_s_barrier(); asm volatile("" ::: "memory"); } while (0)
; #define STG_A(b, h, kt) do { const unsigned char* _g = A + (size_t)KT_(kt) * ASTEP; \
;         dma16((const void*)(_g + (size_t)((h) * 128) * ROWB), ROWB ? aoff[0][0] : aoff[h][0], lds_u + SA_(b, h) + dma0); \
;         dma16((const void*)(_g + (size_t)((h) * 128 + 64) * ROWB), ROWB ? aoff[0][0] : aoff[h][1], lds_u + SA_(b, h) + dma1); } while (0)
;     ...
;     if (!ACCUM)
; #pragma unroll
;     for (int ai = 0; ai < 2; ++ai)
; #pragma unroll
;         for (int bj = 0; bj < 2; ++bj)
; #pragma unroll
;             for (int m = 0; m < 4; ++m)
; #pragma unroll
;                 for (int n = 0; n < 2; ++n) acc[ai][bj][m][n] = (f32x4){0.f, 0.f, 0.f, 0.f};
;     STG_B(0, 0, 0); STG_A(0, 0, 0); STG_B(0, 1, 0); STG_A(0, 1, 0);
;     __builtin_amdgcn_s_waitcnt(0);
;     { int wr1 = wid >> 2; asm volatile("" : "+s"(wr1)); if (wr1 == 1) G_BAR; }
;     G_BAR;
;     { const int p1 = (1 < nt) ? 1 : 0; STG_B(1, 0, p1); STG_A(1, 0, p1); STG_B(1, 1, p1); }
;     G_WAIT_V(6); G_BAR;
; template <int EPI>
; __device__ __forceinline__ void gemm_tile_img(const GemmArgs& g, int pm, int pn, int e, int ebase, int ecnt, LAS3 char* lds, int wid, const unsigned char* img, const TileSync& sy, int kh = -1) {
;     ...
;     for (int h = 0; h < 2; ++h)
; #pragma unroll
;         for (int i = 0; i < 2; ++i) {
;             const int rih = (i * 8 + wid) * 8 + (lane >> 3);
;             const int chunk = (lane & 7) ^ ((rih >> 1) & 7);
;             int r = pm * 256 + h * 128 + rih;
;             unsigned grow;
;             if (EPI == 2) { if (r >= ecnt) r = ecnt - 1; grow = (unsigned)(g.list[e * T + r] >> 2); }
;             else if (EPI == 3) { grow = (unsigned)(((g.abase >> 8) + pm) * (16 * 256) + h * 128 + rih); }
;             else grow = (unsigned)r;
;             aoff[h][i] = (EPI == 3) ? (grow * 128u + (unsigned)(chunk * 16)) : (EPI >= 2) ? (grow * (unsigned)D + (unsigned)(chunk * 16)) : (grow * (unsigned)D + (unsigned)(chunk * 8)) * 2u;
.LBB0_467:
	s_or_b64 exec, exec, s[0:1]
	v_lshrrev_b32_e32 v1, 1, v2
	v_xor_b32_e32 v1, v1, v0
	v_lshlrev_b32_e32 v1, 4, v1
	s_waitcnt vmcnt(3)
	v_lshlrev_b32_e32 v2, 9, v3
	v_and_b32_e32 v1, 0x70, v1
	s_movk_i32 s0, 0xf800
	v_and_or_b32 v144, v2, s0, v1
	s_waitcnt vmcnt(2)
	v_lshlrev_b32_e32 v2, 9, v4
	v_and_or_b32 v152, v2, s0, v1
	s_waitcnt vmcnt(1)
	v_lshlrev_b32_e32 v2, 9, v5
	v_and_or_b32 v153, v2, s0, v1
	s_waitcnt vmcnt(0)
	v_lshlrev_b32_e32 v2, 9, v6
	s_or_b32 s4, s4, s24
	v_readlane_b32 s36, v254, 20
	v_and_or_b32 v154, v2, s0, v1
	s_lshl_b64 s[0:1], s[4:5], 19
	v_readlane_b32 s42, v254, 26
	s_add_u32 s4, s42, s0
	v_and_b32_e32 v1, 63, v0
	v_lshlrev_b32_e32 v3, 3, v0
	s_movk_i32 s0, 0x70
	v_and_b32_e32 v2, 15, v0
	v_bitop3_b32 v0, v3, v0, 63 bitop3:0x78
	v_bitop3_b32 v3, v3, s0, v1 bitop3:0x48
	v_readlane_b32 s0, v254, 60
	v_readlane_b32 s43, v254, 27
	s_addc_u32 vcc_lo, s43, s1
	v_or_b32_e32 v4, s0, v2
	v_readlane_b32 s0, v254, 61
	v_bitop3_b32 v0, v0, 64, v156 bitop3:0x6c
	s_waitcnt lgkmcnt(0)
	v_lshl_add_u32 v2, v2, 7, s0
	s_add_i32 s0, 0, 0x10000
	v_add_u32_e32 v155, v2, v3
	v_add_u32_e32 v156, v2, v0
	v_lshl_add_u32 v2, v4, 7, s0
	s_add_u32 s0, s4, s91
	v_add_u32_e32 v157, v2, v3
	v_add_u32_e32 v158, v2, v0
	s_addc_u32 s1, vcc_lo, s93
	s_barrier
	v_lshlrev_b32_e32 v159, 4, v1
	s_mov_b32 s25, m0
	s_mov_b32 m0, s78
	s_nop 2
	global_load_lds_dwordx4 v159, s[0:1]
	s_mov_b32 m0, s25
	s_add_u32 s0, s4, s92
	s_addc_u32 s1, vcc_lo, s96
	s_mov_b32 s25, m0
	s_mov_b32 m0, s69
	s_nop 2
	global_load_lds_dwordx4 v159, s[0:1]
	s_mov_b32 m0, s25
	s_mov_b32 s0, m0
	s_mov_b32 m0, s94
	s_nop 2
	global_load_lds_dwordx4 v144, s[62:63]
	s_mov_b32 m0, s0
	s_add_u32 s25, s4, 0x4000
	s_mov_b32 s0, m0
	s_mov_b32 m0, s72
	s_nop 2
	global_load_lds_dwordx4 v152, s[62:63]
	s_mov_b32 m0, s0
	s_addc_u32 s28, vcc_lo, 0
	s_add_u32 s0, s25, s91
	s_addc_u32 s1, s28, s93
	s_mov_b32 s29, m0
	s_mov_b32 m0, s70
	s_nop 2
	global_load_lds_dwordx4 v159, s[0:1]
	s_mov_b32 m0, s29
	s_add_u32 s0, s25, s92
	s_addc_u32 s1, s28, s96
	s_mov_b32 s25, m0
	s_mov_b32 m0, s71
	s_nop 2
	global_load_lds_dwordx4 v159, s[0:1]
	s_mov_b32 m0, s25
	s_mov_b32 s0, m0
	s_mov_b32 m0, s61
	s_nop 2
	global_load_lds_dwordx4 v153, s[62:63]
	s_mov_b32 m0, s0
	v_writelane_b32 v255, s74, 24
	s_mov_b32 s0, m0
	s_mov_b32 m0, s59
	s_nop 2
	global_load_lds_dwordx4 v154, s[62:63]
	s_mov_b32 m0, s0
	s_mov_b32 s0, s77
	v_writelane_b32 v255, s73, 25
	v_mov_b32_e32 v145, 0x70
	v_mov_b32_e32 v16, 0
	v_mov_b32_e32 v17, v16
	v_mov_b32_e32 v18, v16
	v_mov_b32_e32 v19, v16
	v_mov_b32_e32 v24, v16
	v_mov_b32_e32 v25, v16
	v_mov_b32_e32 v26, v16
	v_mov_b32_e32 v27, v16
	v_mov_b32_e32 v32, v16
	v_mov_b32_e32 v33, v16
	v_mov_b32_e32 v34, v16
	v_mov_b32_e32 v35, v16
	v_mov_b32_e32 v40, v16
	v_mov_b32_e32 v41, v16
	v_mov_b32_e32 v42, v16
	v_mov_b32_e32 v43, v16
	v_mov_b32_e32 v48, v16
	v_mov_b32_e32 v49, v16
	v_mov_b32_e32 v50, v16
	v_mov_b32_e32 v51, v16
	v_mov_b32_e32 v56, v16
	v_mov_b32_e32 v57, v16
	v_mov_b32_e32 v58, v16
	v_mov_b32_e32 v59, v16
	v_mov_b32_e32 v64, v16
	v_mov_b32_e32 v65, v16
	v_mov_b32_e32 v66, v16
	v_mov_b32_e32 v67, v16
	v_mov_b32_e32 v72, v16
	v_mov_b32_e32 v73, v16
	v_mov_b32_e32 v74, v16
	v_mov_b32_e32 v75, v16
	v_mov_b32_e32 v240, v16
	v_mov_b32_e32 v241, v16
	v_mov_b32_e32 v242, v16
	v_mov_b32_e32 v243, v16
	v_mov_b32_e32 v28, v16
	v_mov_b32_e32 v29, v16
	v_mov_b32_e32 v30, v16
	v_mov_b32_e32 v31, v16
	v_mov_b32_e32 v36, v16
	v_mov_b32_e32 v37, v16
	v_mov_b32_e32 v38, v16
	v_mov_b32_e32 v39, v16
	v_mov_b32_e32 v44, v16
	v_mov_b32_e32 v45, v16
	v_mov_b32_e32 v46, v16
	v_mov_b32_e32 v47, v16
	v_mov_b32_e32 v52, v16
	v_mov_b32_e32 v53, v16
	v_mov_b32_e32 v54, v16
	v_mov_b32_e32 v55, v16
	v_mov_b32_e32 v60, v16
	v_mov_b32_e32 v61, v16
	v_mov_b32_e32 v62, v16
	v_mov_b32_e32 v63, v16
	v_mov_b32_e32 v68, v16
	v_mov_b32_e32 v69, v16
	v_mov_b32_e32 v70, v16
	v_mov_b32_e32 v71, v16
	v_mov_b32_e32 v76, v16
	v_mov_b32_e32 v77, v16
	v_mov_b32_e32 v78, v16
	v_mov_b32_e32 v79, v16
	v_mov_b32_e32 v20, v16
	v_mov_b32_e32 v21, v16
	v_mov_b32_e32 v22, v16
	v_mov_b32_e32 v23, v16
	v_mov_b32_e32 v88, v16
	v_mov_b32_e32 v89, v16
	v_mov_b32_e32 v90, v16
	v_mov_b32_e32 v91, v16
	v_mov_b32_e32 v96, v16
	v_mov_b32_e32 v97, v16
	v_mov_b32_e32 v98, v16
	v_mov_b32_e32 v99, v16
	v_mov_b32_e32 v104, v16
	v_mov_b32_e32 v105, v16
	v_mov_b32_e32 v106, v16
	v_mov_b32_e32 v107, v16
	v_mov_b32_e32 v112, v16
	v_mov_b32_e32 v113, v16
	v_mov_b32_e32 v114, v16
	v_mov_b32_e32 v115, v16
	v_mov_b32_e32 v120, v16
	v_mov_b32_e32 v121, v16
	v_mov_b32_e32 v122, v16
	v_mov_b32_e32 v123, v16
	v_mov_b32_e32 v128, v16
	v_mov_b32_e32 v129, v16
	v_mov_b32_e32 v130, v16
	v_mov_b32_e32 v131, v16
	v_mov_b32_e32 v136, v16
	v_mov_b32_e32 v137, v16
	v_mov_b32_e32 v138, v16
	v_mov_b32_e32 v139, v16
	v_mov_b32_e32 v84, v16
	v_mov_b32_e32 v85, v16
	v_mov_b32_e32 v86, v16
	v_mov_b32_e32 v87, v16
	v_mov_b32_e32 v92, v16
	v_mov_b32_e32 v93, v16
	v_mov_b32_e32 v94, v16
	v_mov_b32_e32 v95, v16
	v_mov_b32_e32 v100, v16
	v_mov_b32_e32 v101, v16
	v_mov_b32_e32 v102, v16
	v_mov_b32_e32 v103, v16
	v_mov_b32_e32 v108, v16
	v_mov_b32_e32 v109, v16
	v_mov_b32_e32 v110, v16
	v_mov_b32_e32 v111, v16
	v_mov_b32_e32 v116, v16
	v_mov_b32_e32 v117, v16
	v_mov_b32_e32 v118, v16
	v_mov_b32_e32 v119, v16
	v_mov_b32_e32 v124, v16
	v_mov_b32_e32 v125, v16
	v_mov_b32_e32 v126, v16
	v_mov_b32_e32 v127, v16
	v_mov_b32_e32 v132, v16
	v_mov_b32_e32 v133, v16
	v_mov_b32_e32 v134, v16
	v_mov_b32_e32 v135, v16
	v_mov_b32_e32 v140, v16
	v_mov_b32_e32 v141, v16
	v_mov_b32_e32 v142, v16
	v_mov_b32_e32 v143, v16
	s_waitcnt vmcnt(0) expcnt(0) lgkmcnt(0)
	s_cmp_lg_u32 s0, 1
	v_readlane_b32 s37, v254, 21
	v_readlane_b32 s38, v254, 22
	v_readlane_b32 s39, v254, 23
	v_readlane_b32 s40, v254, 24
	v_readlane_b32 s41, v254, 25
	v_readlane_b32 s44, v254, 28
	v_readlane_b32 s45, v254, 29
	v_readlane_b32 s46, v254, 30
	v_readlane_b32 s47, v254, 31
	v_readlane_b32 s48, v254, 32
	v_readlane_b32 s49, v254, 33
	v_readlane_b32 s50, v254, 34
	v_readlane_b32 s51, v254, 35
	s_cbranch_scc1 .LBB0_469
	s_barrier
; #define G_WAIT_V(n) asm volatile("s_waitcnt vmcnt(" #n ")" ::: "memory")
; #define G_BAR do { asm volatile("" ::: "memory"); __builtin_amdgcn_s_barrier(); asm volatile("" ::: "memory"); } while (0)
; #define STG_A(b, h, kt) do { const unsigned char* _g = A + (size_t)KT_(kt) * ASTEP; \
;         dma16((const void*)(_g + (size_t)((h) * 128) * ROWB), ROWB ? aoff[0][0] : aoff[h][0], lds_u + SA_(b, h) + dma0); \
;         dma16((const void*)(_g + (size_t)((h) * 128 + 64) * ROWB), ROWB ? aoff[0][0] : aoff[h][1], lds_u + SA_(b, h) + dma1); } while (0)
; #define STG_B(b, h, kt) do { const unsigned char* _g = img + (size_t)KT_(kt) * 32768 + (h) * 16384; \
;         dma16((const void*)(_g + dma0), boffl, lds_u + SB_(b, h) + dma0); \
;         dma16((const void*)(_g + dma1), boffl, lds_u + SB_(b, h) + dma1); } while (0)
;     ...
;     { const int p1 = (1 < nt) ? 1 : 0; STG_B(1, 0, p1); STG_A(1, 0, p1); STG_B(1, 1, p1); }
;     G_WAIT_V(6); G_BAR;
;     for (int t = 0; t < nt; t += 2) {
.LBB0_469:
	s_add_u32 s25, s4, 0x8000
	s_addc_u32 s28, vcc_lo, 0
	s_add_u32 s0, s25, s91
	s_barrier
	s_addc_u32 s1, s28, s93
	s_mov_b32 s29, m0
	s_mov_b32 m0, s60
	s_nop 2
	global_load_lds_dwordx4 v159, s[0:1]
	s_mov_b32 m0, s29
	s_add_u32 s0, s25, s92
	s_addc_u32 s1, s28, s96
	s_mov_b32 s25, m0
	s_mov_b32 m0, s68
	s_nop 2
	global_load_lds_dwordx4 v159, s[0:1]
	s_mov_b32 m0, s25
	s_mov_b32 s0, m0
	s_mov_b32 m0, s90
	s_nop 2
	global_load_lds_dwordx4 v144, s[56:57]
	s_mov_b32 m0, s0
	s_add_u32 s25, s4, 0xc000
	s_mov_b32 s0, m0
	s_mov_b32 m0, s88
	s_nop 2
	global_load_lds_dwordx4 v152, s[56:57]
	s_mov_b32 m0, s0
	s_addc_u32 s28, vcc_lo, 0
	s_add_u32 s0, s25, s91
	s_addc_u32 s1, s28, s93
	s_mov_b32 s29, m0
	s_mov_b32 m0, s33
	s_nop 2
	global_load_lds_dwordx4 v159, s[0:1]
	s_mov_b32 m0, s29
	s_add_u32 s0, s25, s92
	s_addc_u32 s1, s28, s96
	s_mov_b32 s25, m0
	s_mov_b32 m0, s6
	s_nop 2
	global_load_lds_dwordx4 v159, s[0:1]
	s_mov_b32 m0, s25
	s_waitcnt vmcnt(6)
	s_barrier
	s_mov_b64 s[40:41], s[56:57]
	s_mov_b32 vcc_hi, 0
	s_mov_b64 s[0:1], s[62:63]
	v_readlane_b32 s38, v254, 62
	v_readlane_b32 s39, v254, 63

; #define G_WAIT_V(n) asm volatile("s_waitcnt vmcnt(" #n ")" ::: "memory")
; #define G_BAR do { asm volatile("" ::: "memory"); __builtin_amdgcn_s_barrier(); asm volatile("" ::: "memory"); } while (0)
; #define STG_A(b, h, kt) do { const unsigned char* _g = A + (size_t)KT_(kt) * ASTEP; \
;         dma16((const void*)(_g + (size_t)((h) * 128) * ROWB), ROWB ? aoff[0][0] : aoff[h][0], lds_u + SA_(b, h) + dma0); \
;         dma16((const void*)(_g + (size_t)((h) * 128 + 64) * ROWB), ROWB ? aoff[0][0] : aoff[h][1], lds_u + SA_(b, h) + dma1); } while (0)
;     ...
;     if (!ACCUM)
; #pragma unroll
;     for (int ai = 0; ai < 2; ++ai)
; #pragma unroll
;         for (int bj = 0; bj < 2; ++bj)
; #pragma unroll
;             for (int m = 0; m < 4; ++m)
; #pragma unroll
;                 for (int n = 0; n < 2; ++n) acc[ai][bj][m][n] = (f32x4){0.f, 0.f, 0.f, 0.f};
;     STG_B(0, 0, 0); STG_A(0, 0, 0); STG_B(0, 1, 0); STG_A(0, 1, 0);
;     __builtin_amdgcn_s_waitcnt(0);
;     { int wr1 = wid >> 2; asm volatile("" : "+s"(wr1)); if (wr1 == 1) G_BAR; }
;     G_BAR;
;     { const int p1 = (1 < nt) ? 1 : 0; STG_B(1, 0, p1); STG_A(1, 0, p1); STG_B(1, 1, p1); }
;     G_WAIT_V(6); G_BAR;
; template <int EPI>
; __device__ __forceinline__ void gemm_tile_img(const GemmArgs& g, int pm, int pn, int e, int ebase, int ecnt, LAS3 char* lds, int wid, const unsigned char* img, const TileSync& sy, int kh = -1) {
;     ...
;     for (int h = 0; h < 2; ++h)
; #pragma unroll
;         for (int i = 0; i < 2; ++i) {
;             const int rih = (i * 8 + wid) * 8 + (lane >> 3);
;             const int chunk = (lane & 7) ^ ((rih >> 1) & 7);
;             int r = pm * 256 + h * 128 + rih;
;             unsigned grow;
;             if (EPI == 2) { if (r >= ecnt) r = ecnt - 1; grow = (unsigned)(g.list[e * T + r] >> 2); }
;             else if (EPI == 3) { grow = (unsigned)(((g.abase >> 8) + pm) * (16 * 256) + h * 128 + rih); }
;             else grow = (unsigned)r;
;             aoff[h][i] = (EPI == 3) ? (grow * 128u + (unsigned)(chunk * 16)) : (EPI >= 2) ? (grow * (unsigned)D + (unsigned)(chunk * 16)) : (grow * (unsigned)D + (unsigned)(chunk * 8)) * 2u;
.LBB0_559:
	v_writelane_b32 v255, s11, 12
	s_or_b64 exec, exec, s[30:31]
	v_lshrrev_b32_e32 v1, 3, v0
	v_readlane_b32 s0, v254, 59
	v_writelane_b32 v254, s63, 40
	s_or_b32 s4, s4, s15
	v_and_or_b32 v1, v1, 7, s0
	s_lshr_b32 s0, s73, 8
	s_add_i32 s0, s0, s63
	v_lshrrev_b32_e32 v2, 1, v1
	v_xor_b32_e32 v2, v2, v0
	s_lshl_b32 s0, s0, 19
	v_readlane_b32 s36, v254, 20
	v_lshl_add_u32 v1, v1, 7, s0
	v_lshlrev_b32_e32 v2, 4, v2
	s_movk_i32 s30, 0x70
	s_lshl_b64 s[0:1], s[4:5], 19
	v_readlane_b32 s44, v254, 28
	v_and_or_b32 v136, v2, s30, v1
	s_add_u32 s4, s44, s0
	v_and_b32_e32 v2, 15, v0
	v_lshlrev_b32_e32 v3, 3, v0
	v_readlane_b32 s0, v254, 60
	v_writelane_b32 v255, s73, 13
	v_readlane_b32 s45, v254, 29
	v_and_b32_e32 v1, 63, v0
	v_bitop3_b32 v0, v3, v0, 63 bitop3:0x78
	s_waitcnt vmcnt(14)
	v_or_b32_e32 v4, s0, v2
	v_readlane_b32 s0, v254, 61
	s_addc_u32 s25, s45, s1
	v_bitop3_b32 v3, v3, s30, v1 bitop3:0x48
	v_bitop3_b32 v0, v0, 64, v147 bitop3:0x6c
	v_lshl_add_u32 v2, v2, 7, s0
	v_readlane_b32 s0, v255, 24
	v_add_u32_e32 v137, v2, v3
	v_add_u32_e32 v138, v2, v0
	v_lshl_add_u32 v2, v4, 7, s0
	s_add_u32 s0, s4, s91
	v_add_u32_e32 v139, v2, v3
	v_add_u32_e32 v140, v2, v0
	s_addc_u32 s1, s25, s93
	s_waitcnt lgkmcnt(0)
	s_barrier
	v_lshlrev_b32_e32 v141, 4, v1
	s_mov_b32 s30, m0
	s_mov_b32 m0, s78
	s_nop 2
	global_load_lds_dwordx4 v141, s[0:1]
	s_mov_b32 m0, s30
	s_add_u32 s0, s4, s92
	s_addc_u32 s1, s25, s96
	s_mov_b32 s30, m0
	s_mov_b32 m0, s69
	s_nop 2
	global_load_lds_dwordx4 v141, s[0:1]
	s_mov_b32 m0, s30
	s_mov_b32 s0, m0
	s_mov_b32 m0, s94
	s_nop 2
	global_load_lds_dwordx4 v136, s[64:65]
	s_mov_b32 m0, s0
	v_readlane_b32 s38, v254, 22
	v_readlane_b32 s30, v255, 2
	v_readlane_b32 s31, v255, 3
	s_mov_b32 s0, m0
	s_mov_b32 m0, s72
	s_nop 2
	global_load_lds_dwordx4 v136, s[30:31]
	s_mov_b32 m0, s0
	s_add_u32 s30, s4, 0x4000
	s_addc_u32 s31, s25, 0
	s_add_u32 s0, s30, s91
	s_addc_u32 s1, s31, s93
	s_mov_b32 s34, m0
	s_mov_b32 m0, s70
	s_nop 2
	global_load_lds_dwordx4 v141, s[0:1]
	s_mov_b32 m0, s34
	s_add_u32 s0, s30, s92
	s_addc_u32 s1, s31, s96
	s_mov_b32 s30, m0
	s_mov_b32 m0, s71
	s_nop 2
	global_load_lds_dwordx4 v141, s[0:1]
	s_mov_b32 m0, s30
	s_mov_b32 s11, s62
	v_readlane_b32 s30, v255, 17
	v_readlane_b32 s31, v255, 18
	s_mov_b32 s0, m0
	s_mov_b32 m0, s61
	s_nop 2
	global_load_lds_dwordx4 v136, s[30:31]
	s_mov_b32 m0, s0
	v_readlane_b32 s30, v255, 19
	v_readlane_b32 s31, v255, 20
	s_mov_b32 s0, m0
	s_mov_b32 m0, s59
	s_nop 2
	global_load_lds_dwordx4 v136, s[30:31]
	s_mov_b32 m0, s0
	s_mov_b32 s0, s77
	v_mov_b32_e32 v8, 0
	v_mov_b32_e32 v9, v8
	v_mov_b32_e32 v10, v8
	v_mov_b32_e32 v11, v8
	v_mov_b32_e32 v12, v8
	v_mov_b32_e32 v13, v8
	v_mov_b32_e32 v14, v8
	v_mov_b32_e32 v15, v8
	v_mov_b32_e32 v16, v8
	v_mov_b32_e32 v17, v8
	v_mov_b32_e32 v18, v8
	v_mov_b32_e32 v19, v8
	v_mov_b32_e32 v20, v8
	v_mov_b32_e32 v21, v8
	v_mov_b32_e32 v22, v8
	v_mov_b32_e32 v23, v8
	v_mov_b32_e32 v32, v8
	v_mov_b32_e32 v33, v8
	v_mov_b32_e32 v34, v8
	v_mov_b32_e32 v35, v8
	v_mov_b32_e32 v36, v8
	v_mov_b32_e32 v37, v8
	v_mov_b32_e32 v38, v8
	v_mov_b32_e32 v39, v8
	v_mov_b32_e32 v48, v8
	v_mov_b32_e32 v49, v8
	v_mov_b32_e32 v50, v8
	v_mov_b32_e32 v51, v8
	v_mov_b32_e32 v56, v8
	v_mov_b32_e32 v57, v8
	v_mov_b32_e32 v58, v8
	v_mov_b32_e32 v59, v8
	v_mov_b32_e32 v24, v8
	v_mov_b32_e32 v25, v8
	v_mov_b32_e32 v26, v8
	v_mov_b32_e32 v27, v8
	v_mov_b32_e32 v28, v8
	v_mov_b32_e32 v29, v8
	v_mov_b32_e32 v30, v8
	v_mov_b32_e32 v31, v8
	v_mov_b32_e32 v40, v8
	v_mov_b32_e32 v41, v8
	v_mov_b32_e32 v42, v8
	v_mov_b32_e32 v43, v8
	v_mov_b32_e32 v44, v8
	v_mov_b32_e32 v45, v8
	v_mov_b32_e32 v46, v8
	v_mov_b32_e32 v47, v8
	v_mov_b32_e32 v52, v8
	v_mov_b32_e32 v53, v8
	v_mov_b32_e32 v54, v8
	v_mov_b32_e32 v55, v8
	v_mov_b32_e32 v60, v8
	v_mov_b32_e32 v61, v8
	v_mov_b32_e32 v62, v8
	v_mov_b32_e32 v63, v8
	v_mov_b32_e32 v64, v8
	v_mov_b32_e32 v65, v8
	v_mov_b32_e32 v66, v8
	v_mov_b32_e32 v67, v8
	v_mov_b32_e32 v68, v8
	v_mov_b32_e32 v69, v8
	v_mov_b32_e32 v70, v8
	v_mov_b32_e32 v71, v8
	v_mov_b32_e32 v72, v8
	v_mov_b32_e32 v73, v8
	v_mov_b32_e32 v74, v8
	v_mov_b32_e32 v75, v8
	v_mov_b32_e32 v76, v8
	v_mov_b32_e32 v77, v8
	v_mov_b32_e32 v78, v8
	v_mov_b32_e32 v79, v8
	v_mov_b32_e32 v80, v8
	v_mov_b32_e32 v81, v8
	v_mov_b32_e32 v82, v8
	v_mov_b32_e32 v83, v8
	v_mov_b32_e32 v88, v8
	v_mov_b32_e32 v89, v8
	v_mov_b32_e32 v90, v8
	v_mov_b32_e32 v91, v8
	v_mov_b32_e32 v96, v8
	v_mov_b32_e32 v97, v8
	v_mov_b32_e32 v98, v8
	v_mov_b32_e32 v99, v8
	v_mov_b32_e32 v104, v8
	v_mov_b32_e32 v105, v8
	v_mov_b32_e32 v106, v8
	v_mov_b32_e32 v107, v8
	v_mov_b32_e32 v112, v8
	v_mov_b32_e32 v113, v8
	v_mov_b32_e32 v114, v8
	v_mov_b32_e32 v115, v8
	v_mov_b32_e32 v120, v8
	v_mov_b32_e32 v121, v8
	v_mov_b32_e32 v122, v8
	v_mov_b32_e32 v123, v8
	v_mov_b32_e32 v84, v8
	v_mov_b32_e32 v85, v8
	v_mov_b32_e32 v86, v8
	v_mov_b32_e32 v87, v8
	v_mov_b32_e32 v92, v8
	v_mov_b32_e32 v93, v8
	v_mov_b32_e32 v94, v8
	v_mov_b32_e32 v95, v8
	v_mov_b32_e32 v100, v8
	v_mov_b32_e32 v101, v8
	v_mov_b32_e32 v102, v8
	v_mov_b32_e32 v103, v8
	v_mov_b32_e32 v108, v8
	v_mov_b32_e32 v109, v8
	v_mov_b32_e32 v110, v8
	v_mov_b32_e32 v111, v8
	v_mov_b32_e32 v116, v8
	v_mov_b32_e32 v117, v8
	v_mov_b32_e32 v118, v8
	v_mov_b32_e32 v119, v8
	v_mov_b32_e32 v124, v8
	v_mov_b32_e32 v125, v8
	v_mov_b32_e32 v126, v8
	v_mov_b32_e32 v127, v8
	v_mov_b32_e32 v128, v8
	v_mov_b32_e32 v129, v8
	v_mov_b32_e32 v130, v8
	v_mov_b32_e32 v131, v8
	v_mov_b32_e32 v132, v8
	v_mov_b32_e32 v133, v8
	v_mov_b32_e32 v134, v8
	v_mov_b32_e32 v135, v8
	s_waitcnt vmcnt(0) expcnt(0) lgkmcnt(0)
	s_mov_b32 s38, s77
	s_cmp_lg_u32 s0, 1
	v_readlane_b32 s37, v254, 21
	v_readlane_b32 s39, v254, 23
	v_readlane_b32 s40, v254, 24
	v_readlane_b32 s41, v254, 25
	v_readlane_b32 s42, v254, 26
	v_readlane_b32 s43, v254, 27
	v_readlane_b32 s46, v254, 30
	v_readlane_b32 s47, v254, 31
	v_readlane_b32 s48, v254, 32
	v_readlane_b32 s49, v254, 33
	v_readlane_b32 s50, v254, 34
	v_readlane_b32 s51, v254, 35
	s_cbranch_scc1 .LBB0_561
	s_barrier
; #define G_WAIT_V(n) asm volatile("s_waitcnt vmcnt(" #n ")" ::: "memory")
; #define G_BAR do { asm volatile("" ::: "memory"); __builtin_amdgcn_s_barrier(); asm volatile("" ::: "memory"); } while (0)
; #define STG_A(b, h, kt) do { const unsigned char* _g = A + (size_t)KT_(kt) * ASTEP; \
;         dma16((const void*)(_g + (size_t)((h) * 128) * ROWB), ROWB ? aoff[0][0] : aoff[h][0], lds_u + SA_(b, h) + dma0); \
;         dma16((const void*)(_g + (size_t)((h) * 128 + 64) * ROWB), ROWB ? aoff[0][0] : aoff[h][1], lds_u + SA_(b, h) + dma1); } while (0)
; #define STG_B(b, h, kt) do { const unsigned char* _g = img + (size_t)KT_(kt) * 32768 + (h) * 16384; \
;         dma16((const void*)(_g + dma0), boffl, lds_u + SB_(b, h) + dma0); \
;         dma16((const void*)(_g + dma1), boffl, lds_u + SB_(b, h) + dma1); } while (0)
;     ...
;     { int wr1 = wid >> 2; asm volatile("" : "+s"(wr1)); if (wr1 == 1) G_BAR; }
;     G_BAR;
;     { const int p1 = (1 < nt) ? 1 : 0; STG_B(1, 0, p1); STG_A(1, 0, p1); STG_B(1, 1, p1); }
;     G_WAIT_V(6); G_BAR;
;     for (int t = 0; t < nt; t += 2) {
.LBB0_561:
	s_add_u32 s30, s4, 0x8000
	s_addc_u32 s31, s25, 0
	s_add_u32 s0, s30, s91
	s_barrier
	s_addc_u32 s1, s31, s93
	s_mov_b32 s34, m0
	s_mov_b32 m0, s60
	s_nop 2
	global_load_lds_dwordx4 v141, s[0:1]
	s_mov_b32 m0, s34
	s_add_u32 s0, s30, s92
	s_addc_u32 s1, s31, s96
	s_mov_b32 s30, m0
	s_mov_b32 m0, s68
	s_nop 2
	global_load_lds_dwordx4 v141, s[0:1]
	s_mov_b32 m0, s30
	v_readlane_b32 s30, v255, 21
	v_readlane_b32 s31, v255, 22
	s_mov_b32 s0, m0
	s_mov_b32 m0, s90
	s_nop 2
	global_load_lds_dwordx4 v136, s[30:31]
	s_mov_b32 m0, s0
	v_readlane_b32 s30, v255, 25
	v_readlane_b32 s31, v255, 26
	s_mov_b32 s0, m0
	s_mov_b32 m0, s88
	s_nop 2
	global_load_lds_dwordx4 v136, s[30:31]
	s_mov_b32 m0, s0
	s_add_u32 s30, s4, 0xc000
	s_addc_u32 s31, s25, 0
	s_add_u32 s0, s30, s91
	s_addc_u32 s1, s31, s93
	s_mov_b32 s34, m0
	s_mov_b32 m0, s33
	s_nop 2
	global_load_lds_dwordx4 v141, s[0:1]
	s_mov_b32 m0, s34
	s_add_u32 s0, s30, s92
	s_addc_u32 s1, s31, s96
	s_mov_b32 s30, m0
	s_mov_b32 m0, s6
	s_nop 2
	global_load_lds_dwordx4 v141, s[0:1]
	s_mov_b32 m0, s30
	s_waitcnt vmcnt(6)
	s_barrier
	s_mov_b32 vcc_hi, 0
	s_mov_b64 s[0:1], 0
	v_readlane_b32 s40, v254, 62
	v_readlane_b32 s41, v254, 63
